# S5 epilogue U2 loads hoisted (16 in flight), dead S5 discretisation removed
# speedup vs baseline: 1.0055x; 1.0055x over previous
; __device__ __forceinline__ void ph_prologue(const Ctx& c) {
;     ...
;     for (int i = gtid; i < 128 * 64; i += gn) {
;         const int g = i >> 6;
;         const float dt = expf(c.in[11][g]), lr = c.in[9][i], li = c.in[10][i];
;         const float mag = expf(lr * dt), ar = mag * cosf(li * dt), ai = mag * sinf(li * dt);
;         const float den = lr * lr + li * li;
;         const float cr = ((ar - 1.0f) * lr + ai * li) / den, ci = (ai * lr - (ar - 1.0f) * li) / den;
;         float pr = ar, pi = ai;
; #pragma unroll
;         for (int s = 0; s < 6; ++s) { const float nr = pr * pr - pi * pi, ni = 2.0f * pr * pi; pr = nr; pi = ni; }
;         float* A4 = WSP(float, WS_S5A) + (size_t)i * 4; A4[0] = ar; A4[1] = ai; A4[2] = pr; A4[3] = pi;
;         float* Bo = WSP(float, WS_S5B) + (size_t)i * 32;
;         for (int ch = 0; ch < 16; ++ch) { const float br = c.in[12][(size_t)i * 16 + ch], bi = c.in[13][(size_t)i * 16 + ch]; Bo[ch] = cr * br - ci * bi; Bo[16 + ch] = cr * bi + ci * br; }
;     }
.LBB0_173:
	s_or_b64 exec, exec, s[4:5]
	s_movk_i32 s0, 0x2000
	v_cmp_gt_i32_e32 vcc, s0, v0
	s_and_saveexec_b64 s[10:11], vcc
	s_branch .LBB0_184

; __device__ __forceinline__ float gelu_tanh(float x) { const float t = x * x; const float p = __builtin_fmaf(t, -0.10294324f, -2.3022082f); return x * __builtin_amdgcn_rcpf(1.0f + __builtin_amdgcn_exp2f(x * p)); }
; __device__ __forceinline__ u32x4 pack8(const float (&v)[8]) { u32x4 w; w.x = pk2(v[0], v[1]); w.y = pk2(v[2], v[3]); w.z = pk2(v[4], v[5]); w.w = pk2(v[6], v[7]); return w; }
;     __device__ __forceinline__ void operator()(const f32x4 (&acc)[2][2][4][2], const pg::Unit& u, int wr, int wc, int fr, int fq) const {
;         const int g = u.e, ch0 = (fq & 1) * 8; float dv[8];
; #pragma unroll
;         for (int q = 0; q < 8; ++q) dv[q] = dsk[g * 16 + ch0 + q];
; #pragma unroll
;         for (int ai = 0; ai < 2; ++ai)
; #pragma unroll
;             for (int m = 0; m < 4; ++m) { const int n = u.pm * 256 + ai * 128 + wr * 64 + m * 16 + fr;
; #pragma unroll
;                 for (int bj = 0; bj < 2; ++bj) { const int t = u.pn * 16 + 8 * bj + 2 * wc + (fq >> 1); const int token = n * 32 + t;
;                     float uu[8], o[8]; unpack8(*(const u32x4*)(U2 + ((size_t)g * T_ + token) * 16 + ch0), uu);
; #pragma unroll
;                     for (int q = 0; q < 8; ++q) o[q] = gelu_tanh(acc[ai][bj][m][q >> 2][q & 3] + dv[q] * uu[q]);
;                     *(u32x4*)(V + (((size_t)n * 128 + g) * 32 + t) * 16 + ch0) = pack8(o); } }
.LBB0_1779:
	s_lshl_b32 s88, s88, 8
	v_lshl_or_b32 v8, s30, 4, v150
	v_readlane_b32 s12, v254, 27
	v_add_u32_e32 v164, s88, v170
	v_ashrrev_i32_e32 v9, 31, v8
	v_readlane_b32 s13, v254, 28
	s_ashr_i32 s31, s30, 31
	v_ashrrev_i32_e32 v165, 31, v164
	v_readlane_b32 s26, v254, 41
	v_readlane_b32 s27, v254, 42
	v_lshl_add_u64 v[12:13], v[8:9], 2, s[12:13]
	s_lshl_b64 s[34:35], s[30:31], 5
	v_lshlrev_b32_e32 v177, 5, v164
	v_lshlrev_b64 v[8:9], 12, v[164:165]
	v_lshl_add_u32 v162, s33, 4, v173
	s_lshl_b64 s[26:27], s[30:31], 19
	v_lshl_add_u64 v[166:167], v[8:9], 0, s[34:35]
	v_add_u32_e32 v8, v177, v162
	v_ashrrev_i32_e32 v9, 31, v8
	s_add_u32 s30, s3, s26
	s_addc_u32 s31, s36, s27
	v_lshlrev_b64 v[8:9], 5, v[8:9]
	v_lshl_add_u64 v[8:9], s[30:31], 0, v[8:9]
	v_lshlrev_b32_e32 v136, 1, v150
	v_lshl_add_u64 v[8:9], v[8:9], 0, v[136:137]
	v_mov_b32_e32 v250, v8
	v_mov_b32_e32 v251, v9
	global_load_dwordx4 v[8:11], v[12:13], off offset:16
	s_nop 0
	global_load_dwordx4 v[12:15], v[12:13], off
	global_load_dwordx4 v[184:187], v[250:251], off
	global_load_dwordx4 v[188:191], v[250:251], off offset:256
	v_add_co_u32_e32 v248, vcc, 0x4000, v250
	s_nop 1
	v_addc_co_u32_e32 v249, vcc, 0, v251, vcc
	global_load_dwordx4 v[192:195], v[248:249], off
	global_load_dwordx4 v[196:199], v[248:249], off offset:256
	v_add_co_u32_e32 v248, vcc, 0x8000, v250
	s_nop 1
	v_addc_co_u32_e32 v249, vcc, 0, v251, vcc
	global_load_dwordx4 v[200:203], v[248:249], off
	global_load_dwordx4 v[204:207], v[248:249], off offset:256
	v_add_co_u32_e32 v248, vcc, 0xc000, v250
	s_nop 1
	v_addc_co_u32_e32 v249, vcc, 0, v251, vcc
	global_load_dwordx4 v[208:211], v[248:249], off
	global_load_dwordx4 v[212:215], v[248:249], off offset:256
	v_add_co_u32_e32 v248, vcc, 0x20000, v250
	s_nop 1
	v_addc_co_u32_e32 v249, vcc, 0, v251, vcc
	global_load_dwordx4 v[216:219], v[248:249], off
	global_load_dwordx4 v[220:223], v[248:249], off offset:256
	v_add_co_u32_e32 v248, vcc, 0x24000, v250
	s_nop 1
	v_addc_co_u32_e32 v249, vcc, 0, v251, vcc
	global_load_dwordx4 v[224:227], v[248:249], off
	global_load_dwordx4 v[228:231], v[248:249], off offset:256
	v_add_co_u32_e32 v248, vcc, 0x28000, v250
	s_nop 1
	v_addc_co_u32_e32 v249, vcc, 0, v251, vcc
	global_load_dwordx4 v[232:235], v[248:249], off
	global_load_dwordx4 v[236:239], v[248:249], off offset:256
	v_add_co_u32_e32 v248, vcc, 0x2c000, v250
	s_nop 1
	v_addc_co_u32_e32 v249, vcc, 0, v251, vcc
	global_load_dwordx4 v[240:243], v[248:249], off
	global_load_dwordx4 v[244:247], v[248:249], off offset:256
	s_nop 0
	s_nop 0
	s_andn2_b64 vcc, exec, s[28:29]
	v_readlane_b32 s14, v254, 29
	v_readlane_b32 s15, v254, 30
	v_readlane_b32 s16, v254, 31
	v_readlane_b32 s17, v254, 32
	v_readlane_b32 s18, v254, 33
	v_readlane_b32 s19, v254, 34
	v_readlane_b32 s20, v254, 35
	v_readlane_b32 s21, v254, 36
	v_readlane_b32 s22, v254, 37
	v_readlane_b32 s23, v254, 38
	v_readlane_b32 s24, v254, 39
	v_readlane_b32 s25, v254, 40
	s_waitcnt vmcnt(15)
	v_mov_b32_e32 v178, v184
	v_mov_b32_e32 v179, v185
	v_mov_b32_e32 v180, v186
	v_mov_b32_e32 v181, v187
	v_lshlrev_b32_e32 v182, 16, v178
	v_and_b32_e32 v183, 0xffff0000, v178
	v_pk_fma_f32 v[132:133], v[12:13], v[182:183], v[132:133]
	v_lshlrev_b32_e32 v178, 16, v179
	v_pk_mul_f32 v[182:183], v[132:133], v[132:133]
	v_and_b32_e32 v179, 0xffff0000, v179
	v_fmamk_f32 v163, v182, 0xbdd2d3e8, v168
	v_mul_f32_e32 v163, v132, v163
	v_exp_f32_e32 v163, v163
	v_pk_fma_f32 v[134:135], v[14:15], v[178:179], v[134:135]
	v_add_f32_e32 v163, 1.0, v163
	v_rcp_f32_e32 v182, v163
	v_fmamk_f32 v163, v183, 0xbdd2d3e8, v168
	v_mul_f32_e32 v163, v133, v163
	v_exp_f32_e32 v163, v163
	v_pk_mul_f32 v[178:179], v[134:135], v[134:135]
	v_add_f32_e32 v163, 1.0, v163
	v_rcp_f32_e32 v183, v163
	v_fmamk_f32 v163, v178, 0xbdd2d3e8, v168
	v_mul_f32_e32 v163, v134, v163
	v_exp_f32_e32 v163, v163
	v_pk_mul_f32 v[132:133], v[132:133], v[182:183]
	v_add_f32_e32 v163, 1.0, v163
	v_rcp_f32_e32 v178, v163
	v_fmamk_f32 v163, v179, 0xbdd2d3e8, v168
	v_mul_f32_e32 v163, v135, v163
	v_exp_f32_e32 v163, v163
	s_nop 0
	v_add_f32_e32 v163, 1.0, v163
	v_rcp_f32_e32 v179, v163
	s_nop 0
	v_pk_mul_f32 v[134:135], v[134:135], v[178:179]
	v_lshlrev_b32_e32 v178, 16, v180
	v_and_b32_e32 v179, 0xffff0000, v180
	v_pk_fma_f32 v[128:129], v[8:9], v[178:179], v[128:129]
	s_nop 0
	v_pk_mul_f32 v[178:179], v[128:129], v[128:129]
	s_nop 0
	v_fmamk_f32 v163, v178, 0xbdd2d3e8, v168
	v_mul_f32_e32 v163, v128, v163
	v_exp_f32_e32 v163, v163
	s_nop 0
	v_add_f32_e32 v163, 1.0, v163
	v_rcp_f32_e32 v178, v163
	v_fmamk_f32 v163, v179, 0xbdd2d3e8, v168
	v_mul_f32_e32 v163, v129, v163
	v_exp_f32_e32 v163, v163
	s_nop 0
	v_add_f32_e32 v163, 1.0, v163
	v_rcp_f32_e32 v179, v163
	v_ashrrev_i32_e32 v163, 31, v162
	v_pk_mul_f32 v[178:179], v[128:129], v[178:179]
	v_lshlrev_b32_e32 v128, 16, v181
	v_and_b32_e32 v129, 0xffff0000, v181
	v_pk_fma_f32 v[128:129], v[10:11], v[128:129], v[130:131]
	s_nop 0
	v_pk_mul_f32 v[130:131], v[128:129], v[128:129]
	s_nop 0
	v_fmamk_f32 v130, v130, 0xbdd2d3e8, v168
	v_fmamk_f32 v131, v131, 0xbdd2d3e8, v168
	v_mul_f32_e32 v130, v128, v130
	v_mul_f32_e32 v131, v129, v131
	v_exp_f32_e32 v130, v130
	v_exp_f32_e32 v131, v131
	v_add_f32_e32 v130, 1.0, v130
	v_add_f32_e32 v131, 1.0, v131
	v_rcp_f32_e32 v130, v130
	v_rcp_f32_e32 v131, v131
	s_nop 0
	v_pk_mul_f32 v[180:181], v[128:129], v[130:131]
	v_cvt_pk_bf16_f32 v128, v132, v133
	v_lshl_add_u64 v[132:133], v[166:167], 0, v[162:163]
	v_lshlrev_b64 v[132:133], 5, v[132:133]
	v_cvt_pk_bf16_f32 v129, v134, v135
	v_cvt_pk_bf16_f32 v130, v178, v179
	v_cvt_pk_bf16_f32 v131, v180, v181
	v_lshl_add_u64 v[132:133], v[152:153], 0, v[132:133]
	global_store_dwordx4 v[132:133], v[128:131], off
	s_nop 1
	v_add_u32_e32 v128, 8, v162
	v_add_u32_e32 v130, v177, v128
	v_ashrrev_i32_e32 v131, 31, v130
	v_lshlrev_b64 v[130:131], 5, v[130:131]
	v_lshl_add_u64 v[130:131], s[30:31], 0, v[130:131]
	v_lshl_add_u64 v[130:131], v[130:131], 0, v[136:137]
	s_waitcnt vmcnt(15)
; __device__ __forceinline__ float gelu_tanh(float x) { const float t = x * x; const float p = __builtin_fmaf(t, -0.10294324f, -2.3022082f); return x * __builtin_amdgcn_rcpf(1.0f + __builtin_amdgcn_exp2f(x * p)); }
; __device__ __forceinline__ u32x4 pack8(const float (&v)[8]) { u32x4 w; w.x = pk2(v[0], v[1]); w.y = pk2(v[2], v[3]); w.z = pk2(v[4], v[5]); w.w = pk2(v[6], v[7]); return w; }
;     __device__ __forceinline__ void operator()(const f32x4 (&acc)[2][2][4][2], const pg::Unit& u, int wr, int wc, int fr, int fq) const {
;         const int g = u.e, ch0 = (fq & 1) * 8; float dv[8];
; #pragma unroll
;         for (int q = 0; q < 8; ++q) dv[q] = dsk[g * 16 + ch0 + q];
; #pragma unroll
;         for (int ai = 0; ai < 2; ++ai)
; #pragma unroll
;             for (int m = 0; m < 4; ++m) { const int n = u.pm * 256 + ai * 128 + wr * 64 + m * 16 + fr;
; #pragma unroll
;                 for (int bj = 0; bj < 2; ++bj) { const int t = u.pn * 16 + 8 * bj + 2 * wc + (fq >> 1); const int token = n * 32 + t;
;                     float uu[8], o[8]; unpack8(*(const u32x4*)(U2 + ((size_t)g * T_ + token) * 16 + ch0), uu);
; #pragma unroll
;                     for (int q = 0; q < 8; ++q) o[q] = gelu_tanh(acc[ai][bj][m][q >> 2][q & 3] + dv[q] * uu[q]);
;                     *(u32x4*)(V + (((size_t)n * 128 + g) * 32 + t) * 16 + ch0) = pack8(o); } }
	v_mov_b32_e32 v130, v188
	v_mov_b32_e32 v131, v189
	v_mov_b32_e32 v132, v190
	v_mov_b32_e32 v133, v191
	v_lshlrev_b32_e32 v134, 16, v130
	v_and_b32_e32 v135, 0xffff0000, v130
	v_pk_fma_f32 v[124:125], v[12:13], v[134:135], v[124:125]
	v_lshlrev_b32_e32 v130, 16, v131
	v_pk_mul_f32 v[134:135], v[124:125], v[124:125]
	v_and_b32_e32 v131, 0xffff0000, v131
	v_fmamk_f32 v129, v134, 0xbdd2d3e8, v168
	v_mul_f32_e32 v129, v124, v129
	v_exp_f32_e32 v129, v129
	v_pk_fma_f32 v[126:127], v[14:15], v[130:131], v[126:127]
	v_add_f32_e32 v129, 1.0, v129
	v_rcp_f32_e32 v134, v129
	v_fmamk_f32 v129, v135, 0xbdd2d3e8, v168
	v_mul_f32_e32 v129, v125, v129
	v_exp_f32_e32 v129, v129
	v_pk_mul_f32 v[130:131], v[126:127], v[126:127]
	v_add_f32_e32 v129, 1.0, v129
	v_rcp_f32_e32 v135, v129
	v_fmamk_f32 v129, v130, 0xbdd2d3e8, v168
	v_mul_f32_e32 v129, v126, v129
	v_exp_f32_e32 v129, v129
	v_pk_mul_f32 v[124:125], v[124:125], v[134:135]
	v_add_f32_e32 v129, 1.0, v129
	v_rcp_f32_e32 v130, v129
	v_fmamk_f32 v129, v131, 0xbdd2d3e8, v168
	v_mul_f32_e32 v129, v127, v129
	v_exp_f32_e32 v129, v129
	s_nop 0
	v_add_f32_e32 v129, 1.0, v129
	v_rcp_f32_e32 v131, v129
	s_nop 0
	v_pk_mul_f32 v[126:127], v[126:127], v[130:131]
	v_lshlrev_b32_e32 v130, 16, v132
	v_and_b32_e32 v131, 0xffff0000, v132
	v_pk_fma_f32 v[120:121], v[8:9], v[130:131], v[120:121]
	s_nop 0
	v_pk_mul_f32 v[130:131], v[120:121], v[120:121]
	s_nop 0
	v_fmamk_f32 v129, v130, 0xbdd2d3e8, v168
	v_mul_f32_e32 v129, v120, v129
	v_exp_f32_e32 v129, v129
	s_nop 0
	v_add_f32_e32 v129, 1.0, v129
	v_rcp_f32_e32 v130, v129
	v_fmamk_f32 v129, v131, 0xbdd2d3e8, v168
	v_mul_f32_e32 v129, v121, v129
	v_exp_f32_e32 v129, v129
	s_nop 0
	v_add_f32_e32 v129, 1.0, v129
	v_rcp_f32_e32 v131, v129
	v_ashrrev_i32_e32 v129, 31, v128
	v_pk_mul_f32 v[130:131], v[120:121], v[130:131]
	v_lshlrev_b32_e32 v120, 16, v133
	v_and_b32_e32 v121, 0xffff0000, v133
	v_pk_fma_f32 v[120:121], v[10:11], v[120:121], v[122:123]
	s_nop 0
	v_pk_mul_f32 v[122:123], v[120:121], v[120:121]
	s_nop 0
	v_fmamk_f32 v122, v122, 0xbdd2d3e8, v168
	v_fmamk_f32 v123, v123, 0xbdd2d3e8, v168
	v_mul_f32_e32 v122, v120, v122
	v_mul_f32_e32 v123, v121, v123
	v_exp_f32_e32 v122, v122
	v_exp_f32_e32 v123, v123
	v_add_f32_e32 v122, 1.0, v122
	v_add_f32_e32 v123, 1.0, v123
	v_rcp_f32_e32 v122, v122
	v_rcp_f32_e32 v123, v123
	s_nop 0
	v_pk_mul_f32 v[132:133], v[120:121], v[122:123]
	v_cvt_pk_bf16_f32 v120, v124, v125
	v_lshl_add_u64 v[124:125], v[166:167], 0, v[128:129]
	v_lshlrev_b64 v[124:125], 5, v[124:125]
	v_cvt_pk_bf16_f32 v121, v126, v127
	v_cvt_pk_bf16_f32 v122, v130, v131
	v_cvt_pk_bf16_f32 v123, v132, v133
	v_lshl_add_u64 v[124:125], v[152:153], 0, v[124:125]
	global_store_dwordx4 v[124:125], v[120:123], off
	s_nop 1
	v_add_u32_e32 v120, s88, v174
	v_lshlrev_b32_e32 v124, 5, v120
	v_add_u32_e32 v122, v124, v162
	v_ashrrev_i32_e32 v123, 31, v122
	v_lshlrev_b64 v[122:123], 5, v[122:123]
	v_lshl_add_u64 v[122:123], s[30:31], 0, v[122:123]
	v_lshl_add_u64 v[122:123], v[122:123], 0, v[136:137]
	v_ashrrev_i32_e32 v121, 31, v120
	v_lshlrev_b64 v[120:121], 12, v[120:121]
	v_lshl_add_u64 v[120:121], v[120:121], 0, s[34:35]
	s_waitcnt vmcnt(15)
	v_mov_b32_e32 v130, v192
	v_mov_b32_e32 v131, v193
	v_mov_b32_e32 v132, v194
	v_mov_b32_e32 v133, v195
	v_lshlrev_b32_e32 v122, 16, v130
	v_and_b32_e32 v123, 0xffff0000, v130
	v_pk_fma_f32 v[116:117], v[12:13], v[122:123], v[116:117]
	s_nop 0
	v_pk_mul_f32 v[122:123], v[116:117], v[116:117]
	s_nop 0
	v_fmamk_f32 v122, v122, 0xbdd2d3e8, v168
	v_fmamk_f32 v123, v123, 0xbdd2d3e8, v168
	v_mul_f32_e32 v122, v116, v122
	v_mul_f32_e32 v123, v117, v123
	v_exp_f32_e32 v122, v122
	v_exp_f32_e32 v123, v123
	v_add_f32_e32 v122, 1.0, v122
	v_add_f32_e32 v123, 1.0, v123
	v_rcp_f32_e32 v122, v122
	v_rcp_f32_e32 v123, v123
	s_nop 0
	v_pk_mul_f32 v[116:117], v[116:117], v[122:123]
	v_lshlrev_b32_e32 v122, 16, v131
	v_and_b32_e32 v123, 0xffff0000, v131
	v_pk_fma_f32 v[118:119], v[14:15], v[122:123], v[118:119]
	s_nop 0
	v_pk_mul_f32 v[122:123], v[118:119], v[118:119]
	s_nop 0
	v_fmamk_f32 v122, v122, 0xbdd2d3e8, v168
	v_fmamk_f32 v123, v123, 0xbdd2d3e8, v168
	v_mul_f32_e32 v122, v118, v122
	v_mul_f32_e32 v123, v119, v123
	v_exp_f32_e32 v122, v122
	v_exp_f32_e32 v123, v123
	v_add_f32_e32 v122, 1.0, v122
	v_add_f32_e32 v123, 1.0, v123
	v_rcp_f32_e32 v122, v122
	v_rcp_f32_e32 v123, v123
	s_nop 0
	v_pk_mul_f32 v[118:119], v[118:119], v[122:123]
	v_lshlrev_b32_e32 v122, 16, v132
	v_and_b32_e32 v123, 0xffff0000, v132
	v_pk_fma_f32 v[112:113], v[8:9], v[122:123], v[112:113]
	s_nop 0
	v_pk_mul_f32 v[122:123], v[112:113], v[112:113]
	s_nop 0
	v_fmamk_f32 v122, v122, 0xbdd2d3e8, v168
	v_fmamk_f32 v123, v123, 0xbdd2d3e8, v168
	v_mul_f32_e32 v122, v112, v122
	v_mul_f32_e32 v123, v113, v123
	v_exp_f32_e32 v122, v122
	v_exp_f32_e32 v123, v123
	v_add_f32_e32 v122, 1.0, v122
	v_add_f32_e32 v123, 1.0, v123
	v_rcp_f32_e32 v122, v122
	v_rcp_f32_e32 v123, v123
	s_nop 0
	v_pk_mul_f32 v[122:123], v[112:113], v[122:123]
	v_lshlrev_b32_e32 v112, 16, v133
	v_and_b32_e32 v113, 0xffff0000, v133
	v_pk_fma_f32 v[112:113], v[10:11], v[112:113], v[114:115]
	s_nop 0
	v_pk_mul_f32 v[114:115], v[112:113], v[112:113]
	s_nop 0
	v_fmamk_f32 v114, v114, 0xbdd2d3e8, v168
	v_fmamk_f32 v115, v115, 0xbdd2d3e8, v168
	v_mul_f32_e32 v114, v112, v114
	v_mul_f32_e32 v115, v113, v115
	v_exp_f32_e32 v114, v114
	v_exp_f32_e32 v115, v115
	v_add_f32_e32 v114, 1.0, v114
	v_add_f32_e32 v115, 1.0, v115
	v_rcp_f32_e32 v114, v114
	v_rcp_f32_e32 v115, v115
	s_nop 0
	v_pk_mul_f32 v[126:127], v[112:113], v[114:115]
	v_cvt_pk_bf16_f32 v112, v116, v117
	v_lshl_add_u64 v[116:117], v[120:121], 0, v[162:163]
	v_lshlrev_b64 v[116:117], 5, v[116:117]
	v_cvt_pk_bf16_f32 v113, v118, v119
	v_cvt_pk_bf16_f32 v114, v122, v123
	v_cvt_pk_bf16_f32 v115, v126, v127
	v_lshl_add_u64 v[116:117], v[152:153], 0, v[116:117]
	global_store_dwordx4 v[116:117], v[112:115], off
	s_nop 1
	v_add_u32_e32 v112, v124, v128
	v_ashrrev_i32_e32 v113, 31, v112
	v_lshlrev_b64 v[112:113], 5, v[112:113]
	v_lshl_add_u64 v[112:113], s[30:31], 0, v[112:113]
	v_lshl_add_u64 v[112:113], v[112:113], 0, v[136:137]
	s_waitcnt vmcnt(15)
; __device__ __forceinline__ float gelu_tanh(float x) { const float t = x * x; const float p = __builtin_fmaf(t, -0.10294324f, -2.3022082f); return x * __builtin_amdgcn_rcpf(1.0f + __builtin_amdgcn_exp2f(x * p)); }
; __device__ __forceinline__ u32x4 pack8(const float (&v)[8]) { u32x4 w; w.x = pk2(v[0], v[1]); w.y = pk2(v[2], v[3]); w.z = pk2(v[4], v[5]); w.w = pk2(v[6], v[7]); return w; }
;     __device__ __forceinline__ void operator()(const f32x4 (&acc)[2][2][4][2], const pg::Unit& u, int wr, int wc, int fr, int fq) const {
;         const int g = u.e, ch0 = (fq & 1) * 8; float dv[8];
; #pragma unroll
;         for (int q = 0; q < 8; ++q) dv[q] = dsk[g * 16 + ch0 + q];
; #pragma unroll
;         for (int ai = 0; ai < 2; ++ai)
; #pragma unroll
;             for (int m = 0; m < 4; ++m) { const int n = u.pm * 256 + ai * 128 + wr * 64 + m * 16 + fr;
; #pragma unroll
;                 for (int bj = 0; bj < 2; ++bj) { const int t = u.pn * 16 + 8 * bj + 2 * wc + (fq >> 1); const int token = n * 32 + t;
;                     float uu[8], o[8]; unpack8(*(const u32x4*)(U2 + ((size_t)g * T_ + token) * 16 + ch0), uu);
; #pragma unroll
;                     for (int q = 0; q < 8; ++q) o[q] = gelu_tanh(acc[ai][bj][m][q >> 2][q & 3] + dv[q] * uu[q]);
;                     *(u32x4*)(V + (((size_t)n * 128 + g) * 32 + t) * 16 + ch0) = pack8(o); } }
	v_mov_b32_e32 v112, v196
	v_mov_b32_e32 v113, v197
	v_mov_b32_e32 v114, v198
	v_mov_b32_e32 v115, v199
	v_lshlrev_b32_e32 v116, 16, v112
	v_and_b32_e32 v117, 0xffff0000, v112
	v_pk_fma_f32 v[108:109], v[12:13], v[116:117], v[108:109]
	s_nop 0
	v_pk_mul_f32 v[116:117], v[108:109], v[108:109]
	s_nop 0
	v_fmamk_f32 v112, v116, 0xbdd2d3e8, v168
	v_mul_f32_e32 v112, v108, v112
	v_exp_f32_e32 v112, v112
	s_nop 0
	v_add_f32_e32 v112, 1.0, v112
	v_rcp_f32_e32 v116, v112
	v_fmamk_f32 v112, v117, 0xbdd2d3e8, v168
	v_mul_f32_e32 v112, v109, v112
	v_exp_f32_e32 v112, v112
	s_nop 0
	v_add_f32_e32 v112, 1.0, v112
	v_rcp_f32_e32 v117, v112
	v_lshlrev_b32_e32 v112, 16, v113
	v_and_b32_e32 v113, 0xffff0000, v113
	v_pk_fma_f32 v[110:111], v[14:15], v[112:113], v[110:111]
	v_pk_mul_f32 v[108:109], v[108:109], v[116:117]
	v_pk_mul_f32 v[112:113], v[110:111], v[110:111]
	s_nop 0
	v_fmamk_f32 v112, v112, 0xbdd2d3e8, v168
	v_fmamk_f32 v113, v113, 0xbdd2d3e8, v168
	v_mul_f32_e32 v112, v110, v112
	v_mul_f32_e32 v113, v111, v113
	v_exp_f32_e32 v112, v112
	v_exp_f32_e32 v113, v113
	v_add_f32_e32 v112, 1.0, v112
	v_add_f32_e32 v113, 1.0, v113
	v_rcp_f32_e32 v112, v112
	v_rcp_f32_e32 v113, v113
	s_nop 0
	v_pk_mul_f32 v[110:111], v[110:111], v[112:113]
	v_lshlrev_b32_e32 v112, 16, v114
	v_and_b32_e32 v113, 0xffff0000, v114
	v_pk_fma_f32 v[104:105], v[8:9], v[112:113], v[104:105]
	s_nop 0
	v_pk_mul_f32 v[112:113], v[104:105], v[104:105]
	s_nop 0
	v_fmamk_f32 v112, v112, 0xbdd2d3e8, v168
	v_fmamk_f32 v113, v113, 0xbdd2d3e8, v168
	v_mul_f32_e32 v112, v104, v112
	v_mul_f32_e32 v113, v105, v113
	v_exp_f32_e32 v112, v112
	v_exp_f32_e32 v113, v113
	v_add_f32_e32 v112, 1.0, v112
	v_add_f32_e32 v113, 1.0, v113
	v_rcp_f32_e32 v112, v112
	v_rcp_f32_e32 v113, v113
	s_nop 0
	v_pk_mul_f32 v[112:113], v[104:105], v[112:113]
	v_lshlrev_b32_e32 v104, 16, v115
	v_and_b32_e32 v105, 0xffff0000, v115
	v_pk_fma_f32 v[104:105], v[10:11], v[104:105], v[106:107]
	s_nop 0
	v_pk_mul_f32 v[106:107], v[104:105], v[104:105]
	s_nop 0
	v_fmamk_f32 v106, v106, 0xbdd2d3e8, v168
	v_fmamk_f32 v107, v107, 0xbdd2d3e8, v168
	v_mul_f32_e32 v106, v104, v106
	v_mul_f32_e32 v107, v105, v107
	v_exp_f32_e32 v106, v106
	v_exp_f32_e32 v107, v107
	v_add_f32_e32 v106, 1.0, v106
	v_add_f32_e32 v107, 1.0, v107
	v_rcp_f32_e32 v106, v106
	v_rcp_f32_e32 v107, v107
	s_nop 0
	v_pk_mul_f32 v[114:115], v[104:105], v[106:107]
	v_cvt_pk_bf16_f32 v104, v108, v109
	v_lshl_add_u64 v[108:109], v[120:121], 0, v[128:129]
	v_lshlrev_b64 v[108:109], 5, v[108:109]
	v_cvt_pk_bf16_f32 v105, v110, v111
	v_cvt_pk_bf16_f32 v106, v112, v113
	v_cvt_pk_bf16_f32 v107, v114, v115
	v_lshl_add_u64 v[108:109], v[152:153], 0, v[108:109]
	global_store_dwordx4 v[108:109], v[104:107], off
	s_nop 1
	v_add_u32_e32 v104, s88, v175
	v_lshlrev_b32_e32 v108, 5, v104
	v_add_u32_e32 v106, v108, v162
	v_ashrrev_i32_e32 v107, 31, v106
	v_lshlrev_b64 v[106:107], 5, v[106:107]
	v_lshl_add_u64 v[106:107], s[30:31], 0, v[106:107]
	v_lshl_add_u64 v[106:107], v[106:107], 0, v[136:137]
	v_ashrrev_i32_e32 v105, 31, v104
	v_lshlrev_b64 v[104:105], 12, v[104:105]
	v_lshl_add_u64 v[104:105], v[104:105], 0, s[34:35]
	s_waitcnt vmcnt(15)
	v_mov_b32_e32 v110, v200
	v_mov_b32_e32 v111, v201
	v_mov_b32_e32 v112, v202
	v_mov_b32_e32 v113, v203
	v_lshlrev_b32_e32 v106, 16, v110
	v_and_b32_e32 v107, 0xffff0000, v110
	v_pk_fma_f32 v[100:101], v[12:13], v[106:107], v[100:101]
	s_nop 0
	v_pk_mul_f32 v[106:107], v[100:101], v[100:101]
	s_nop 0
	v_fmamk_f32 v106, v106, 0xbdd2d3e8, v168
	v_fmamk_f32 v107, v107, 0xbdd2d3e8, v168
	v_mul_f32_e32 v106, v100, v106
	v_mul_f32_e32 v107, v101, v107
	v_exp_f32_e32 v106, v106
	v_exp_f32_e32 v107, v107
	v_add_f32_e32 v106, 1.0, v106
	v_add_f32_e32 v107, 1.0, v107
	v_rcp_f32_e32 v106, v106
	v_rcp_f32_e32 v107, v107
	s_nop 0
	v_pk_mul_f32 v[100:101], v[100:101], v[106:107]
	v_lshlrev_b32_e32 v106, 16, v111
	v_and_b32_e32 v107, 0xffff0000, v111
	v_pk_fma_f32 v[102:103], v[14:15], v[106:107], v[102:103]
	s_nop 0
	v_pk_mul_f32 v[106:107], v[102:103], v[102:103]
	s_nop 0
	v_fmamk_f32 v106, v106, 0xbdd2d3e8, v168
	v_fmamk_f32 v107, v107, 0xbdd2d3e8, v168
	v_mul_f32_e32 v106, v102, v106
	v_mul_f32_e32 v107, v103, v107
	v_exp_f32_e32 v106, v106
	v_exp_f32_e32 v107, v107
	v_add_f32_e32 v106, 1.0, v106
	v_add_f32_e32 v107, 1.0, v107
	v_rcp_f32_e32 v106, v106
	v_rcp_f32_e32 v107, v107
	s_nop 0
	v_pk_mul_f32 v[102:103], v[102:103], v[106:107]
	v_lshlrev_b32_e32 v106, 16, v112
	v_and_b32_e32 v107, 0xffff0000, v112
	v_pk_fma_f32 v[96:97], v[8:9], v[106:107], v[96:97]
	s_nop 0
	v_pk_mul_f32 v[106:107], v[96:97], v[96:97]
	s_nop 0
	v_fmamk_f32 v106, v106, 0xbdd2d3e8, v168
	v_fmamk_f32 v107, v107, 0xbdd2d3e8, v168
	v_mul_f32_e32 v106, v96, v106
	v_mul_f32_e32 v107, v97, v107
	v_exp_f32_e32 v106, v106
	v_exp_f32_e32 v107, v107
	v_add_f32_e32 v106, 1.0, v106
	v_add_f32_e32 v107, 1.0, v107
	v_rcp_f32_e32 v106, v106
	v_rcp_f32_e32 v107, v107
	s_nop 0
	v_pk_mul_f32 v[106:107], v[96:97], v[106:107]
	v_lshlrev_b32_e32 v96, 16, v113
	v_and_b32_e32 v97, 0xffff0000, v113
	v_pk_fma_f32 v[96:97], v[10:11], v[96:97], v[98:99]
	s_nop 0
	v_pk_mul_f32 v[98:99], v[96:97], v[96:97]
	s_nop 0
	v_fmamk_f32 v98, v98, 0xbdd2d3e8, v168
	v_fmamk_f32 v99, v99, 0xbdd2d3e8, v168
	v_mul_f32_e32 v98, v96, v98
	v_mul_f32_e32 v99, v97, v99
	v_exp_f32_e32 v98, v98
	v_exp_f32_e32 v99, v99
	v_add_f32_e32 v98, 1.0, v98
	v_add_f32_e32 v99, 1.0, v99
	v_rcp_f32_e32 v98, v98
	v_rcp_f32_e32 v99, v99
	s_nop 0
	v_pk_mul_f32 v[110:111], v[96:97], v[98:99]
	v_cvt_pk_bf16_f32 v96, v100, v101
	v_lshl_add_u64 v[100:101], v[104:105], 0, v[162:163]
	v_lshlrev_b64 v[100:101], 5, v[100:101]
	v_cvt_pk_bf16_f32 v97, v102, v103
	v_cvt_pk_bf16_f32 v98, v106, v107
	v_cvt_pk_bf16_f32 v99, v110, v111
	v_lshl_add_u64 v[100:101], v[152:153], 0, v[100:101]
	global_store_dwordx4 v[100:101], v[96:99], off
	s_nop 1
	v_add_u32_e32 v96, v108, v128
	v_ashrrev_i32_e32 v97, 31, v96
	v_lshlrev_b64 v[96:97], 5, v[96:97]
	v_lshl_add_u64 v[96:97], s[30:31], 0, v[96:97]
	v_lshl_add_u64 v[96:97], v[96:97], 0, v[136:137]
	s_waitcnt vmcnt(15)
; __device__ __forceinline__ float gelu_tanh(float x) { const float t = x * x; const float p = __builtin_fmaf(t, -0.10294324f, -2.3022082f); return x * __builtin_amdgcn_rcpf(1.0f + __builtin_amdgcn_exp2f(x * p)); }
; __device__ __forceinline__ u32x4 pack8(const float (&v)[8]) { u32x4 w; w.x = pk2(v[0], v[1]); w.y = pk2(v[2], v[3]); w.z = pk2(v[4], v[5]); w.w = pk2(v[6], v[7]); return w; }
;     __device__ __forceinline__ void operator()(const f32x4 (&acc)[2][2][4][2], const pg::Unit& u, int wr, int wc, int fr, int fq) const {
;         const int g = u.e, ch0 = (fq & 1) * 8; float dv[8];
; #pragma unroll
;         for (int q = 0; q < 8; ++q) dv[q] = dsk[g * 16 + ch0 + q];
; #pragma unroll
;         for (int ai = 0; ai < 2; ++ai)
; #pragma unroll
;             for (int m = 0; m < 4; ++m) { const int n = u.pm * 256 + ai * 128 + wr * 64 + m * 16 + fr;
; #pragma unroll
;                 for (int bj = 0; bj < 2; ++bj) { const int t = u.pn * 16 + 8 * bj + 2 * wc + (fq >> 1); const int token = n * 32 + t;
;                     float uu[8], o[8]; unpack8(*(const u32x4*)(U2 + ((size_t)g * T_ + token) * 16 + ch0), uu);
; #pragma unroll
;                     for (int q = 0; q < 8; ++q) o[q] = gelu_tanh(acc[ai][bj][m][q >> 2][q & 3] + dv[q] * uu[q]);
;                     *(u32x4*)(V + (((size_t)n * 128 + g) * 32 + t) * 16 + ch0) = pack8(o); } }
	v_mov_b32_e32 v96, v204
	v_mov_b32_e32 v97, v205
	v_mov_b32_e32 v98, v206
	v_mov_b32_e32 v99, v207
	v_lshlrev_b32_e32 v100, 16, v96
	v_and_b32_e32 v101, 0xffff0000, v96
	v_pk_fma_f32 v[92:93], v[12:13], v[100:101], v[92:93]
	s_nop 0
	v_pk_mul_f32 v[100:101], v[92:93], v[92:93]
	s_nop 0
	v_fmamk_f32 v96, v100, 0xbdd2d3e8, v168
	v_mul_f32_e32 v96, v92, v96
	v_exp_f32_e32 v96, v96
	s_nop 0
	v_add_f32_e32 v96, 1.0, v96
	v_rcp_f32_e32 v100, v96
	v_fmamk_f32 v96, v101, 0xbdd2d3e8, v168
	v_mul_f32_e32 v96, v93, v96
	v_exp_f32_e32 v96, v96
	s_nop 0
	v_add_f32_e32 v96, 1.0, v96
	v_rcp_f32_e32 v101, v96
	v_lshlrev_b32_e32 v96, 16, v97
	v_and_b32_e32 v97, 0xffff0000, v97
	v_pk_fma_f32 v[94:95], v[14:15], v[96:97], v[94:95]
	v_pk_mul_f32 v[92:93], v[92:93], v[100:101]
	v_pk_mul_f32 v[96:97], v[94:95], v[94:95]
	s_nop 0
	v_fmamk_f32 v96, v96, 0xbdd2d3e8, v168
	v_fmamk_f32 v97, v97, 0xbdd2d3e8, v168
	v_mul_f32_e32 v96, v94, v96
	v_mul_f32_e32 v97, v95, v97
	v_exp_f32_e32 v96, v96
	v_exp_f32_e32 v97, v97
	v_add_f32_e32 v96, 1.0, v96
	v_add_f32_e32 v97, 1.0, v97
	v_rcp_f32_e32 v96, v96
	v_rcp_f32_e32 v97, v97
	s_nop 0
	v_pk_mul_f32 v[94:95], v[94:95], v[96:97]
	v_lshlrev_b32_e32 v96, 16, v98
	v_and_b32_e32 v97, 0xffff0000, v98
	v_pk_fma_f32 v[88:89], v[8:9], v[96:97], v[88:89]
	s_nop 0
	v_pk_mul_f32 v[96:97], v[88:89], v[88:89]
	s_nop 0
	v_fmamk_f32 v96, v96, 0xbdd2d3e8, v168
	v_fmamk_f32 v97, v97, 0xbdd2d3e8, v168
	v_mul_f32_e32 v96, v88, v96
	v_mul_f32_e32 v97, v89, v97
	v_exp_f32_e32 v96, v96
	v_exp_f32_e32 v97, v97
	v_add_f32_e32 v96, 1.0, v96
	v_add_f32_e32 v97, 1.0, v97
	v_rcp_f32_e32 v96, v96
	v_rcp_f32_e32 v97, v97
	s_nop 0
	v_pk_mul_f32 v[96:97], v[88:89], v[96:97]
	v_lshlrev_b32_e32 v88, 16, v99
	v_and_b32_e32 v89, 0xffff0000, v99
	v_pk_fma_f32 v[88:89], v[10:11], v[88:89], v[90:91]
	s_nop 0
	v_pk_mul_f32 v[90:91], v[88:89], v[88:89]
	s_nop 0
	v_fmamk_f32 v90, v90, 0xbdd2d3e8, v168
	v_fmamk_f32 v91, v91, 0xbdd2d3e8, v168
	v_mul_f32_e32 v90, v88, v90
	v_mul_f32_e32 v91, v89, v91
	v_exp_f32_e32 v90, v90
	v_exp_f32_e32 v91, v91
	v_add_f32_e32 v90, 1.0, v90
	v_add_f32_e32 v91, 1.0, v91
	v_rcp_f32_e32 v90, v90
	v_rcp_f32_e32 v91, v91
	s_nop 0
	v_pk_mul_f32 v[98:99], v[88:89], v[90:91]
	v_cvt_pk_bf16_f32 v88, v92, v93
	v_lshl_add_u64 v[92:93], v[104:105], 0, v[128:129]
	v_lshlrev_b64 v[92:93], 5, v[92:93]
	v_cvt_pk_bf16_f32 v89, v94, v95
	v_cvt_pk_bf16_f32 v90, v96, v97
	v_cvt_pk_bf16_f32 v91, v98, v99
	v_lshl_add_u64 v[92:93], v[152:153], 0, v[92:93]
	global_store_dwordx4 v[92:93], v[88:91], off
	s_nop 1
	v_add_u32_e32 v88, s88, v176
	v_lshlrev_b32_e32 v92, 5, v88
	v_add_u32_e32 v90, v92, v162
	v_ashrrev_i32_e32 v91, 31, v90
	v_lshlrev_b64 v[90:91], 5, v[90:91]
	v_lshl_add_u64 v[90:91], s[30:31], 0, v[90:91]
	v_lshl_add_u64 v[90:91], v[90:91], 0, v[136:137]
	v_ashrrev_i32_e32 v89, 31, v88
	v_lshlrev_b64 v[88:89], 12, v[88:89]
	v_lshl_add_u64 v[88:89], v[88:89], 0, s[34:35]
	s_waitcnt vmcnt(15)
	v_mov_b32_e32 v94, v208
	v_mov_b32_e32 v95, v209
	v_mov_b32_e32 v96, v210
	v_mov_b32_e32 v97, v211
	v_lshlrev_b32_e32 v90, 16, v94
	v_and_b32_e32 v91, 0xffff0000, v94
	v_pk_fma_f32 v[84:85], v[12:13], v[90:91], v[84:85]
	s_nop 0
	v_pk_mul_f32 v[90:91], v[84:85], v[84:85]
	s_nop 0
	v_fmamk_f32 v90, v90, 0xbdd2d3e8, v168
	v_fmamk_f32 v91, v91, 0xbdd2d3e8, v168
	v_mul_f32_e32 v90, v84, v90
	v_mul_f32_e32 v91, v85, v91
	v_exp_f32_e32 v90, v90
	v_exp_f32_e32 v91, v91
	v_add_f32_e32 v90, 1.0, v90
	v_add_f32_e32 v91, 1.0, v91
	v_rcp_f32_e32 v90, v90
	v_rcp_f32_e32 v91, v91
	s_nop 0
	v_pk_mul_f32 v[84:85], v[84:85], v[90:91]
	v_lshlrev_b32_e32 v90, 16, v95
	v_and_b32_e32 v91, 0xffff0000, v95
	v_pk_fma_f32 v[86:87], v[14:15], v[90:91], v[86:87]
	s_nop 0
	v_pk_mul_f32 v[90:91], v[86:87], v[86:87]
	s_nop 0
	v_fmamk_f32 v90, v90, 0xbdd2d3e8, v168
	v_fmamk_f32 v91, v91, 0xbdd2d3e8, v168
	v_mul_f32_e32 v90, v86, v90
	v_mul_f32_e32 v91, v87, v91
	v_exp_f32_e32 v90, v90
	v_exp_f32_e32 v91, v91
	v_add_f32_e32 v90, 1.0, v90
	v_add_f32_e32 v91, 1.0, v91
	v_rcp_f32_e32 v90, v90
	v_rcp_f32_e32 v91, v91
	s_nop 0
	v_pk_mul_f32 v[86:87], v[86:87], v[90:91]
	v_lshlrev_b32_e32 v90, 16, v96
	v_and_b32_e32 v91, 0xffff0000, v96
	v_pk_fma_f32 v[80:81], v[8:9], v[90:91], v[80:81]
	s_nop 0
	v_pk_mul_f32 v[90:91], v[80:81], v[80:81]
	s_nop 0
	v_fmamk_f32 v90, v90, 0xbdd2d3e8, v168
	v_fmamk_f32 v91, v91, 0xbdd2d3e8, v168
	v_mul_f32_e32 v90, v80, v90
	v_mul_f32_e32 v91, v81, v91
	v_exp_f32_e32 v90, v90
	v_exp_f32_e32 v91, v91
	v_add_f32_e32 v90, 1.0, v90
	v_add_f32_e32 v91, 1.0, v91
	v_rcp_f32_e32 v90, v90
	v_rcp_f32_e32 v91, v91
	s_nop 0
	v_pk_mul_f32 v[90:91], v[80:81], v[90:91]
	v_lshlrev_b32_e32 v80, 16, v97
	v_and_b32_e32 v81, 0xffff0000, v97
	v_pk_fma_f32 v[80:81], v[10:11], v[80:81], v[82:83]
	s_nop 0
	v_pk_mul_f32 v[82:83], v[80:81], v[80:81]
	s_nop 0
	v_fmamk_f32 v82, v82, 0xbdd2d3e8, v168
	v_fmamk_f32 v83, v83, 0xbdd2d3e8, v168
	v_mul_f32_e32 v82, v80, v82
	v_mul_f32_e32 v83, v81, v83
	v_exp_f32_e32 v82, v82
	v_exp_f32_e32 v83, v83
	v_add_f32_e32 v82, 1.0, v82
	v_add_f32_e32 v83, 1.0, v83
	v_rcp_f32_e32 v82, v82
	v_rcp_f32_e32 v83, v83
	s_nop 0
	v_pk_mul_f32 v[94:95], v[80:81], v[82:83]
	v_cvt_pk_bf16_f32 v80, v84, v85
	v_lshl_add_u64 v[84:85], v[88:89], 0, v[162:163]
	v_lshlrev_b64 v[84:85], 5, v[84:85]
	v_cvt_pk_bf16_f32 v81, v86, v87
	v_cvt_pk_bf16_f32 v82, v90, v91
	v_cvt_pk_bf16_f32 v83, v94, v95
	v_lshl_add_u64 v[84:85], v[152:153], 0, v[84:85]
	global_store_dwordx4 v[84:85], v[80:83], off
	s_nop 1
	v_add_u32_e32 v80, v92, v128
	v_ashrrev_i32_e32 v81, 31, v80
	v_lshlrev_b64 v[80:81], 5, v[80:81]
	v_lshl_add_u64 v[80:81], s[30:31], 0, v[80:81]
	v_lshl_add_u64 v[80:81], v[80:81], 0, v[136:137]
	s_waitcnt vmcnt(15)
; __device__ __forceinline__ float gelu_tanh(float x) { const float t = x * x; const float p = __builtin_fmaf(t, -0.10294324f, -2.3022082f); return x * __builtin_amdgcn_rcpf(1.0f + __builtin_amdgcn_exp2f(x * p)); }
; __device__ __forceinline__ u32x4 pack8(const float (&v)[8]) { u32x4 w; w.x = pk2(v[0], v[1]); w.y = pk2(v[2], v[3]); w.z = pk2(v[4], v[5]); w.w = pk2(v[6], v[7]); return w; }
;     __device__ __forceinline__ void operator()(const f32x4 (&acc)[2][2][4][2], const pg::Unit& u, int wr, int wc, int fr, int fq) const {
;         const int g = u.e, ch0 = (fq & 1) * 8; float dv[8];
; #pragma unroll
;         for (int q = 0; q < 8; ++q) dv[q] = dsk[g * 16 + ch0 + q];
; #pragma unroll
;         for (int ai = 0; ai < 2; ++ai)
; #pragma unroll
;             for (int m = 0; m < 4; ++m) { const int n = u.pm * 256 + ai * 128 + wr * 64 + m * 16 + fr;
; #pragma unroll
;                 for (int bj = 0; bj < 2; ++bj) { const int t = u.pn * 16 + 8 * bj + 2 * wc + (fq >> 1); const int token = n * 32 + t;
;                     float uu[8], o[8]; unpack8(*(const u32x4*)(U2 + ((size_t)g * T_ + token) * 16 + ch0), uu);
; #pragma unroll
;                     for (int q = 0; q < 8; ++q) o[q] = gelu_tanh(acc[ai][bj][m][q >> 2][q & 3] + dv[q] * uu[q]);
;                     *(u32x4*)(V + (((size_t)n * 128 + g) * 32 + t) * 16 + ch0) = pack8(o); } }
	v_mov_b32_e32 v80, v212
	v_mov_b32_e32 v81, v213
	v_mov_b32_e32 v82, v214
	v_mov_b32_e32 v83, v215
	v_lshlrev_b32_e32 v84, 16, v80
	v_and_b32_e32 v85, 0xffff0000, v80
	v_pk_fma_f32 v[76:77], v[12:13], v[84:85], v[76:77]
	s_nop 0
	v_pk_mul_f32 v[84:85], v[76:77], v[76:77]
	s_nop 0
	v_fmamk_f32 v80, v84, 0xbdd2d3e8, v168
	v_mul_f32_e32 v80, v76, v80
	v_exp_f32_e32 v80, v80
	s_nop 0
	v_add_f32_e32 v80, 1.0, v80
	v_rcp_f32_e32 v84, v80
	v_fmamk_f32 v80, v85, 0xbdd2d3e8, v168
	v_mul_f32_e32 v80, v77, v80
	v_exp_f32_e32 v80, v80
	s_nop 0
	v_add_f32_e32 v80, 1.0, v80
	v_rcp_f32_e32 v85, v80
	v_lshlrev_b32_e32 v80, 16, v81
	v_and_b32_e32 v81, 0xffff0000, v81
	v_pk_fma_f32 v[78:79], v[14:15], v[80:81], v[78:79]
	v_pk_mul_f32 v[76:77], v[76:77], v[84:85]
	v_pk_mul_f32 v[80:81], v[78:79], v[78:79]
	s_nop 0
	v_fmamk_f32 v80, v80, 0xbdd2d3e8, v168
	v_fmamk_f32 v81, v81, 0xbdd2d3e8, v168
	v_mul_f32_e32 v80, v78, v80
	v_mul_f32_e32 v81, v79, v81
	v_exp_f32_e32 v80, v80
	v_exp_f32_e32 v81, v81
	v_add_f32_e32 v80, 1.0, v80
	v_add_f32_e32 v81, 1.0, v81
	v_rcp_f32_e32 v80, v80
	v_rcp_f32_e32 v81, v81
	s_nop 0
	v_pk_mul_f32 v[78:79], v[78:79], v[80:81]
	v_lshlrev_b32_e32 v80, 16, v82
	v_and_b32_e32 v81, 0xffff0000, v82
	v_pk_fma_f32 v[72:73], v[8:9], v[80:81], v[72:73]
	s_nop 0
	v_pk_mul_f32 v[80:81], v[72:73], v[72:73]
	s_nop 0
	v_fmamk_f32 v80, v80, 0xbdd2d3e8, v168
	v_fmamk_f32 v81, v81, 0xbdd2d3e8, v168
	v_mul_f32_e32 v80, v72, v80
	v_mul_f32_e32 v81, v73, v81
	v_exp_f32_e32 v80, v80
	v_exp_f32_e32 v81, v81
	v_add_f32_e32 v80, 1.0, v80
	v_add_f32_e32 v81, 1.0, v81
	v_rcp_f32_e32 v80, v80
	v_rcp_f32_e32 v81, v81
	s_nop 0
	v_pk_mul_f32 v[80:81], v[72:73], v[80:81]
	v_lshlrev_b32_e32 v72, 16, v83
	v_and_b32_e32 v73, 0xffff0000, v83
	v_pk_fma_f32 v[72:73], v[10:11], v[72:73], v[74:75]
	s_nop 0
	v_pk_mul_f32 v[74:75], v[72:73], v[72:73]
	s_nop 0
	v_fmamk_f32 v74, v74, 0xbdd2d3e8, v168
	v_fmamk_f32 v75, v75, 0xbdd2d3e8, v168
	v_mul_f32_e32 v74, v72, v74
	v_mul_f32_e32 v75, v73, v75
	v_exp_f32_e32 v74, v74
	v_exp_f32_e32 v75, v75
	v_add_f32_e32 v74, 1.0, v74
	v_add_f32_e32 v75, 1.0, v75
	v_rcp_f32_e32 v74, v74
	v_rcp_f32_e32 v75, v75
	s_nop 0
	v_pk_mul_f32 v[82:83], v[72:73], v[74:75]
	v_cvt_pk_bf16_f32 v72, v76, v77
	v_lshl_add_u64 v[76:77], v[88:89], 0, v[128:129]
	v_lshlrev_b64 v[76:77], 5, v[76:77]
	v_cvt_pk_bf16_f32 v73, v78, v79
	v_cvt_pk_bf16_f32 v74, v80, v81
	v_cvt_pk_bf16_f32 v75, v82, v83
	v_lshl_add_u64 v[76:77], v[152:153], 0, v[76:77]
	global_store_dwordx4 v[76:77], v[72:75], off
	s_nop 1
	v_add_u32_e32 v72, 0x80, v164
	v_lshlrev_b32_e32 v76, 5, v72
	v_add_u32_e32 v74, v76, v162
	v_ashrrev_i32_e32 v75, 31, v74
	v_lshlrev_b64 v[74:75], 5, v[74:75]
	v_lshl_add_u64 v[74:75], s[30:31], 0, v[74:75]
	v_lshl_add_u64 v[74:75], v[74:75], 0, v[136:137]
	v_ashrrev_i32_e32 v73, 31, v72
	v_lshlrev_b64 v[72:73], 12, v[72:73]
	v_lshl_add_u64 v[72:73], v[72:73], 0, s[34:35]
	s_waitcnt vmcnt(15)
	v_mov_b32_e32 v78, v216
	v_mov_b32_e32 v79, v217
	v_mov_b32_e32 v80, v218
	v_mov_b32_e32 v81, v219
	v_lshlrev_b32_e32 v74, 16, v78
	v_and_b32_e32 v75, 0xffff0000, v78
	v_pk_fma_f32 v[68:69], v[12:13], v[74:75], v[68:69]
	s_nop 0
	v_pk_mul_f32 v[74:75], v[68:69], v[68:69]
	s_nop 0
	v_fmamk_f32 v74, v74, 0xbdd2d3e8, v168
	v_fmamk_f32 v75, v75, 0xbdd2d3e8, v168
	v_mul_f32_e32 v74, v68, v74
	v_mul_f32_e32 v75, v69, v75
	v_exp_f32_e32 v74, v74
	v_exp_f32_e32 v75, v75
	v_add_f32_e32 v74, 1.0, v74
	v_add_f32_e32 v75, 1.0, v75
	v_rcp_f32_e32 v74, v74
	v_rcp_f32_e32 v75, v75
	s_nop 0
	v_pk_mul_f32 v[68:69], v[68:69], v[74:75]
	v_lshlrev_b32_e32 v74, 16, v79
	v_and_b32_e32 v75, 0xffff0000, v79
	v_pk_fma_f32 v[70:71], v[14:15], v[74:75], v[70:71]
	s_nop 0
	v_pk_mul_f32 v[74:75], v[70:71], v[70:71]
	s_nop 0
	v_fmamk_f32 v74, v74, 0xbdd2d3e8, v168
	v_fmamk_f32 v75, v75, 0xbdd2d3e8, v168
	v_mul_f32_e32 v74, v70, v74
	v_mul_f32_e32 v75, v71, v75
	v_exp_f32_e32 v74, v74
	v_exp_f32_e32 v75, v75
	v_add_f32_e32 v74, 1.0, v74
	v_add_f32_e32 v75, 1.0, v75
	v_rcp_f32_e32 v74, v74
	v_rcp_f32_e32 v75, v75
	s_nop 0
	v_pk_mul_f32 v[70:71], v[70:71], v[74:75]
	v_lshlrev_b32_e32 v74, 16, v80
	v_and_b32_e32 v75, 0xffff0000, v80
	v_pk_fma_f32 v[64:65], v[8:9], v[74:75], v[64:65]
	s_nop 0
	v_pk_mul_f32 v[74:75], v[64:65], v[64:65]
	s_nop 0
	v_fmamk_f32 v74, v74, 0xbdd2d3e8, v168
	v_fmamk_f32 v75, v75, 0xbdd2d3e8, v168
	v_mul_f32_e32 v74, v64, v74
	v_mul_f32_e32 v75, v65, v75
	v_exp_f32_e32 v74, v74
	v_exp_f32_e32 v75, v75
	v_add_f32_e32 v74, 1.0, v74
	v_add_f32_e32 v75, 1.0, v75
	v_rcp_f32_e32 v74, v74
	v_rcp_f32_e32 v75, v75
	s_nop 0
	v_pk_mul_f32 v[74:75], v[64:65], v[74:75]
	v_lshlrev_b32_e32 v64, 16, v81
	v_and_b32_e32 v65, 0xffff0000, v81
	v_pk_fma_f32 v[64:65], v[10:11], v[64:65], v[66:67]
	s_nop 0
	v_pk_mul_f32 v[66:67], v[64:65], v[64:65]
	s_nop 0
	v_fmamk_f32 v66, v66, 0xbdd2d3e8, v168
	v_fmamk_f32 v67, v67, 0xbdd2d3e8, v168
	v_mul_f32_e32 v66, v64, v66
	v_mul_f32_e32 v67, v65, v67
	v_exp_f32_e32 v66, v66
	v_exp_f32_e32 v67, v67
	v_add_f32_e32 v66, 1.0, v66
	v_add_f32_e32 v67, 1.0, v67
	v_rcp_f32_e32 v66, v66
	v_rcp_f32_e32 v67, v67
	s_nop 0
	v_pk_mul_f32 v[78:79], v[64:65], v[66:67]
	v_cvt_pk_bf16_f32 v64, v68, v69
	v_lshl_add_u64 v[68:69], v[72:73], 0, v[162:163]
	v_lshlrev_b64 v[68:69], 5, v[68:69]
	v_cvt_pk_bf16_f32 v65, v70, v71
	v_cvt_pk_bf16_f32 v66, v74, v75
	v_cvt_pk_bf16_f32 v67, v78, v79
	v_lshl_add_u64 v[68:69], v[152:153], 0, v[68:69]
	global_store_dwordx4 v[68:69], v[64:67], off
	s_nop 1
	v_add_u32_e32 v64, v76, v128
	v_ashrrev_i32_e32 v65, 31, v64
	v_lshlrev_b64 v[64:65], 5, v[64:65]
	v_lshl_add_u64 v[64:65], s[30:31], 0, v[64:65]
	v_lshl_add_u64 v[64:65], v[64:65], 0, v[136:137]
	s_waitcnt vmcnt(15)
; __device__ __forceinline__ float gelu_tanh(float x) { const float t = x * x; const float p = __builtin_fmaf(t, -0.10294324f, -2.3022082f); return x * __builtin_amdgcn_rcpf(1.0f + __builtin_amdgcn_exp2f(x * p)); }
; __device__ __forceinline__ u32x4 pack8(const float (&v)[8]) { u32x4 w; w.x = pk2(v[0], v[1]); w.y = pk2(v[2], v[3]); w.z = pk2(v[4], v[5]); w.w = pk2(v[6], v[7]); return w; }
;     __device__ __forceinline__ void operator()(const f32x4 (&acc)[2][2][4][2], const pg::Unit& u, int wr, int wc, int fr, int fq) const {
;         const int g = u.e, ch0 = (fq & 1) * 8; float dv[8];
; #pragma unroll
;         for (int q = 0; q < 8; ++q) dv[q] = dsk[g * 16 + ch0 + q];
; #pragma unroll
;         for (int ai = 0; ai < 2; ++ai)
; #pragma unroll
;             for (int m = 0; m < 4; ++m) { const int n = u.pm * 256 + ai * 128 + wr * 64 + m * 16 + fr;
; #pragma unroll
;                 for (int bj = 0; bj < 2; ++bj) { const int t = u.pn * 16 + 8 * bj + 2 * wc + (fq >> 1); const int token = n * 32 + t;
;                     float uu[8], o[8]; unpack8(*(const u32x4*)(U2 + ((size_t)g * T_ + token) * 16 + ch0), uu);
; #pragma unroll
;                     for (int q = 0; q < 8; ++q) o[q] = gelu_tanh(acc[ai][bj][m][q >> 2][q & 3] + dv[q] * uu[q]);
;                     *(u32x4*)(V + (((size_t)n * 128 + g) * 32 + t) * 16 + ch0) = pack8(o); } }
	v_mov_b32_e32 v64, v220
	v_mov_b32_e32 v65, v221
	v_mov_b32_e32 v66, v222
	v_mov_b32_e32 v67, v223
	v_lshlrev_b32_e32 v68, 16, v64
	v_and_b32_e32 v69, 0xffff0000, v64
	v_pk_fma_f32 v[60:61], v[12:13], v[68:69], v[60:61]
	s_nop 0
	v_pk_mul_f32 v[68:69], v[60:61], v[60:61]
	s_nop 0
	v_fmamk_f32 v64, v68, 0xbdd2d3e8, v168
	v_mul_f32_e32 v64, v60, v64
	v_exp_f32_e32 v64, v64
	s_nop 0
	v_add_f32_e32 v64, 1.0, v64
	v_rcp_f32_e32 v68, v64
	v_fmamk_f32 v64, v69, 0xbdd2d3e8, v168
	v_mul_f32_e32 v64, v61, v64
	v_exp_f32_e32 v64, v64
	s_nop 0
	v_add_f32_e32 v64, 1.0, v64
	v_rcp_f32_e32 v69, v64
	v_lshlrev_b32_e32 v64, 16, v65
	v_and_b32_e32 v65, 0xffff0000, v65
	v_pk_fma_f32 v[62:63], v[14:15], v[64:65], v[62:63]
	v_pk_mul_f32 v[60:61], v[60:61], v[68:69]
	v_pk_mul_f32 v[64:65], v[62:63], v[62:63]
	s_nop 0
	v_fmamk_f32 v64, v64, 0xbdd2d3e8, v168
	v_fmamk_f32 v65, v65, 0xbdd2d3e8, v168
	v_mul_f32_e32 v64, v62, v64
	v_mul_f32_e32 v65, v63, v65
	v_exp_f32_e32 v64, v64
	v_exp_f32_e32 v65, v65
	v_add_f32_e32 v64, 1.0, v64
	v_add_f32_e32 v65, 1.0, v65
	v_rcp_f32_e32 v64, v64
	v_rcp_f32_e32 v65, v65
	s_nop 0
	v_pk_mul_f32 v[62:63], v[62:63], v[64:65]
	v_lshlrev_b32_e32 v64, 16, v66
	v_and_b32_e32 v65, 0xffff0000, v66
	v_pk_fma_f32 v[56:57], v[8:9], v[64:65], v[56:57]
	s_nop 0
	v_pk_mul_f32 v[64:65], v[56:57], v[56:57]
	s_nop 0
	v_fmamk_f32 v64, v64, 0xbdd2d3e8, v168
	v_fmamk_f32 v65, v65, 0xbdd2d3e8, v168
	v_mul_f32_e32 v64, v56, v64
	v_mul_f32_e32 v65, v57, v65
	v_exp_f32_e32 v64, v64
	v_exp_f32_e32 v65, v65
	v_add_f32_e32 v64, 1.0, v64
	v_add_f32_e32 v65, 1.0, v65
	v_rcp_f32_e32 v64, v64
	v_rcp_f32_e32 v65, v65
	s_nop 0
	v_pk_mul_f32 v[64:65], v[56:57], v[64:65]
	v_lshlrev_b32_e32 v56, 16, v67
	v_and_b32_e32 v57, 0xffff0000, v67
	v_pk_fma_f32 v[56:57], v[10:11], v[56:57], v[58:59]
	s_nop 0
	v_pk_mul_f32 v[58:59], v[56:57], v[56:57]
	s_nop 0
	v_fmamk_f32 v58, v58, 0xbdd2d3e8, v168
	v_fmamk_f32 v59, v59, 0xbdd2d3e8, v168
	v_mul_f32_e32 v58, v56, v58
	v_mul_f32_e32 v59, v57, v59
	v_exp_f32_e32 v58, v58
	v_exp_f32_e32 v59, v59
	v_add_f32_e32 v58, 1.0, v58
	v_add_f32_e32 v59, 1.0, v59
	v_rcp_f32_e32 v58, v58
	v_rcp_f32_e32 v59, v59
	s_nop 0
	v_pk_mul_f32 v[66:67], v[56:57], v[58:59]
	v_cvt_pk_bf16_f32 v56, v60, v61
	v_lshl_add_u64 v[60:61], v[72:73], 0, v[128:129]
	v_lshlrev_b64 v[60:61], 5, v[60:61]
	v_cvt_pk_bf16_f32 v57, v62, v63
	v_cvt_pk_bf16_f32 v58, v64, v65
	v_cvt_pk_bf16_f32 v59, v66, v67
	v_lshl_add_u64 v[60:61], v[152:153], 0, v[60:61]
	global_store_dwordx4 v[60:61], v[56:59], off
	s_nop 1
	v_add_u32_e32 v56, 0x90, v164
	v_lshlrev_b32_e32 v60, 5, v56
	v_add_u32_e32 v58, v60, v162
	v_ashrrev_i32_e32 v59, 31, v58
	v_lshlrev_b64 v[58:59], 5, v[58:59]
	v_lshl_add_u64 v[58:59], s[30:31], 0, v[58:59]
	v_lshl_add_u64 v[58:59], v[58:59], 0, v[136:137]
	v_ashrrev_i32_e32 v57, 31, v56
	v_lshlrev_b64 v[56:57], 12, v[56:57]
	v_lshl_add_u64 v[56:57], v[56:57], 0, s[34:35]
	s_waitcnt vmcnt(15)
	v_mov_b32_e32 v62, v224
	v_mov_b32_e32 v63, v225
	v_mov_b32_e32 v64, v226
	v_mov_b32_e32 v65, v227
	v_lshlrev_b32_e32 v58, 16, v62
	v_and_b32_e32 v59, 0xffff0000, v62
	v_pk_fma_f32 v[52:53], v[12:13], v[58:59], v[52:53]
	s_nop 0
	v_pk_mul_f32 v[58:59], v[52:53], v[52:53]
	s_nop 0
	v_fmamk_f32 v58, v58, 0xbdd2d3e8, v168
	v_fmamk_f32 v59, v59, 0xbdd2d3e8, v168
	v_mul_f32_e32 v58, v52, v58
	v_mul_f32_e32 v59, v53, v59
	v_exp_f32_e32 v58, v58
	v_exp_f32_e32 v59, v59
	v_add_f32_e32 v58, 1.0, v58
	v_add_f32_e32 v59, 1.0, v59
	v_rcp_f32_e32 v58, v58
	v_rcp_f32_e32 v59, v59
	s_nop 0
	v_pk_mul_f32 v[52:53], v[52:53], v[58:59]
	v_lshlrev_b32_e32 v58, 16, v63
	v_and_b32_e32 v59, 0xffff0000, v63
	v_pk_fma_f32 v[54:55], v[14:15], v[58:59], v[54:55]
	s_nop 0
	v_pk_mul_f32 v[58:59], v[54:55], v[54:55]
	s_nop 0
	v_fmamk_f32 v58, v58, 0xbdd2d3e8, v168
	v_fmamk_f32 v59, v59, 0xbdd2d3e8, v168
	v_mul_f32_e32 v58, v54, v58
	v_mul_f32_e32 v59, v55, v59
	v_exp_f32_e32 v58, v58
	v_exp_f32_e32 v59, v59
	v_add_f32_e32 v58, 1.0, v58
	v_add_f32_e32 v59, 1.0, v59
	v_rcp_f32_e32 v58, v58
	v_rcp_f32_e32 v59, v59
	s_nop 0
	v_pk_mul_f32 v[54:55], v[54:55], v[58:59]
	v_lshlrev_b32_e32 v58, 16, v64
	v_and_b32_e32 v59, 0xffff0000, v64
	v_pk_fma_f32 v[48:49], v[8:9], v[58:59], v[48:49]
	s_nop 0
	v_pk_mul_f32 v[58:59], v[48:49], v[48:49]
	s_nop 0
	v_fmamk_f32 v58, v58, 0xbdd2d3e8, v168
	v_fmamk_f32 v59, v59, 0xbdd2d3e8, v168
	v_mul_f32_e32 v58, v48, v58
	v_mul_f32_e32 v59, v49, v59
	v_exp_f32_e32 v58, v58
	v_exp_f32_e32 v59, v59
	v_add_f32_e32 v58, 1.0, v58
	v_add_f32_e32 v59, 1.0, v59
	v_rcp_f32_e32 v58, v58
	v_rcp_f32_e32 v59, v59
	s_nop 0
	v_pk_mul_f32 v[58:59], v[48:49], v[58:59]
	v_lshlrev_b32_e32 v48, 16, v65
	v_and_b32_e32 v49, 0xffff0000, v65
	v_pk_fma_f32 v[48:49], v[10:11], v[48:49], v[50:51]
	s_nop 0
	v_pk_mul_f32 v[50:51], v[48:49], v[48:49]
	s_nop 0
	v_fmamk_f32 v50, v50, 0xbdd2d3e8, v168
	v_fmamk_f32 v51, v51, 0xbdd2d3e8, v168
	v_mul_f32_e32 v50, v48, v50
	v_mul_f32_e32 v51, v49, v51
	v_exp_f32_e32 v50, v50
	v_exp_f32_e32 v51, v51
	v_add_f32_e32 v50, 1.0, v50
	v_add_f32_e32 v51, 1.0, v51
	v_rcp_f32_e32 v50, v50
	v_rcp_f32_e32 v51, v51
	s_nop 0
	v_pk_mul_f32 v[62:63], v[48:49], v[50:51]
	v_cvt_pk_bf16_f32 v48, v52, v53
	v_lshl_add_u64 v[52:53], v[56:57], 0, v[162:163]
	v_lshlrev_b64 v[52:53], 5, v[52:53]
	v_cvt_pk_bf16_f32 v49, v54, v55
	v_cvt_pk_bf16_f32 v50, v58, v59
	v_cvt_pk_bf16_f32 v51, v62, v63
	v_lshl_add_u64 v[52:53], v[152:153], 0, v[52:53]
	global_store_dwordx4 v[52:53], v[48:51], off
	s_nop 1
	v_add_u32_e32 v48, v60, v128
	v_ashrrev_i32_e32 v49, 31, v48
	v_lshlrev_b64 v[48:49], 5, v[48:49]
	v_lshl_add_u64 v[48:49], s[30:31], 0, v[48:49]
	v_lshl_add_u64 v[48:49], v[48:49], 0, v[136:137]
	s_waitcnt vmcnt(15)
; __device__ __forceinline__ float gelu_tanh(float x) { const float t = x * x; const float p = __builtin_fmaf(t, -0.10294324f, -2.3022082f); return x * __builtin_amdgcn_rcpf(1.0f + __builtin_amdgcn_exp2f(x * p)); }
; __device__ __forceinline__ u32x4 pack8(const float (&v)[8]) { u32x4 w; w.x = pk2(v[0], v[1]); w.y = pk2(v[2], v[3]); w.z = pk2(v[4], v[5]); w.w = pk2(v[6], v[7]); return w; }
;     __device__ __forceinline__ void operator()(const f32x4 (&acc)[2][2][4][2], const pg::Unit& u, int wr, int wc, int fr, int fq) const {
;         const int g = u.e, ch0 = (fq & 1) * 8; float dv[8];
; #pragma unroll
;         for (int q = 0; q < 8; ++q) dv[q] = dsk[g * 16 + ch0 + q];
; #pragma unroll
;         for (int ai = 0; ai < 2; ++ai)
; #pragma unroll
;             for (int m = 0; m < 4; ++m) { const int n = u.pm * 256 + ai * 128 + wr * 64 + m * 16 + fr;
; #pragma unroll
;                 for (int bj = 0; bj < 2; ++bj) { const int t = u.pn * 16 + 8 * bj + 2 * wc + (fq >> 1); const int token = n * 32 + t;
;                     float uu[8], o[8]; unpack8(*(const u32x4*)(U2 + ((size_t)g * T_ + token) * 16 + ch0), uu);
; #pragma unroll
;                     for (int q = 0; q < 8; ++q) o[q] = gelu_tanh(acc[ai][bj][m][q >> 2][q & 3] + dv[q] * uu[q]);
;                     *(u32x4*)(V + (((size_t)n * 128 + g) * 32 + t) * 16 + ch0) = pack8(o); } }
	v_mov_b32_e32 v48, v228
	v_mov_b32_e32 v49, v229
	v_mov_b32_e32 v50, v230
	v_mov_b32_e32 v51, v231
	v_lshlrev_b32_e32 v52, 16, v48
	v_and_b32_e32 v53, 0xffff0000, v48
	v_pk_fma_f32 v[44:45], v[12:13], v[52:53], v[44:45]
	s_nop 0
	v_pk_mul_f32 v[52:53], v[44:45], v[44:45]
	s_nop 0
	v_fmamk_f32 v48, v52, 0xbdd2d3e8, v168
	v_mul_f32_e32 v48, v44, v48
	v_exp_f32_e32 v48, v48
	s_nop 0
	v_add_f32_e32 v48, 1.0, v48
	v_rcp_f32_e32 v52, v48
	v_fmamk_f32 v48, v53, 0xbdd2d3e8, v168
	v_mul_f32_e32 v48, v45, v48
	v_exp_f32_e32 v48, v48
	s_nop 0
	v_add_f32_e32 v48, 1.0, v48
	v_rcp_f32_e32 v53, v48
	v_lshlrev_b32_e32 v48, 16, v49
	v_and_b32_e32 v49, 0xffff0000, v49
	v_pk_fma_f32 v[46:47], v[14:15], v[48:49], v[46:47]
	v_pk_mul_f32 v[44:45], v[44:45], v[52:53]
	v_pk_mul_f32 v[48:49], v[46:47], v[46:47]
	s_nop 0
	v_fmamk_f32 v48, v48, 0xbdd2d3e8, v168
	v_fmamk_f32 v49, v49, 0xbdd2d3e8, v168
	v_mul_f32_e32 v48, v46, v48
	v_mul_f32_e32 v49, v47, v49
	v_exp_f32_e32 v48, v48
	v_exp_f32_e32 v49, v49
	v_add_f32_e32 v48, 1.0, v48
	v_add_f32_e32 v49, 1.0, v49
	v_rcp_f32_e32 v48, v48
	v_rcp_f32_e32 v49, v49
	s_nop 0
	v_pk_mul_f32 v[46:47], v[46:47], v[48:49]
	v_lshlrev_b32_e32 v48, 16, v50
	v_and_b32_e32 v49, 0xffff0000, v50
	v_pk_fma_f32 v[40:41], v[8:9], v[48:49], v[40:41]
	s_nop 0
	v_pk_mul_f32 v[48:49], v[40:41], v[40:41]
	s_nop 0
	v_fmamk_f32 v48, v48, 0xbdd2d3e8, v168
	v_fmamk_f32 v49, v49, 0xbdd2d3e8, v168
	v_mul_f32_e32 v48, v40, v48
	v_mul_f32_e32 v49, v41, v49
	v_exp_f32_e32 v48, v48
	v_exp_f32_e32 v49, v49
	v_add_f32_e32 v48, 1.0, v48
	v_add_f32_e32 v49, 1.0, v49
	v_rcp_f32_e32 v48, v48
	v_rcp_f32_e32 v49, v49
	s_nop 0
	v_pk_mul_f32 v[48:49], v[40:41], v[48:49]
	v_lshlrev_b32_e32 v40, 16, v51
	v_and_b32_e32 v41, 0xffff0000, v51
	v_pk_fma_f32 v[40:41], v[10:11], v[40:41], v[42:43]
	s_nop 0
	v_pk_mul_f32 v[42:43], v[40:41], v[40:41]
	s_nop 0
	v_fmamk_f32 v42, v42, 0xbdd2d3e8, v168
	v_fmamk_f32 v43, v43, 0xbdd2d3e8, v168
	v_mul_f32_e32 v42, v40, v42
	v_mul_f32_e32 v43, v41, v43
	v_exp_f32_e32 v42, v42
	v_exp_f32_e32 v43, v43
	v_add_f32_e32 v42, 1.0, v42
	v_add_f32_e32 v43, 1.0, v43
	v_rcp_f32_e32 v42, v42
	v_rcp_f32_e32 v43, v43
	s_nop 0
	v_pk_mul_f32 v[50:51], v[40:41], v[42:43]
	v_cvt_pk_bf16_f32 v40, v44, v45
	v_lshl_add_u64 v[44:45], v[56:57], 0, v[128:129]
	v_lshlrev_b64 v[44:45], 5, v[44:45]
	v_cvt_pk_bf16_f32 v41, v46, v47
	v_cvt_pk_bf16_f32 v42, v48, v49
	v_cvt_pk_bf16_f32 v43, v50, v51
	v_lshl_add_u64 v[44:45], v[152:153], 0, v[44:45]
	global_store_dwordx4 v[44:45], v[40:43], off
	s_nop 1
	v_add_u32_e32 v40, 0xa0, v164
	v_lshlrev_b32_e32 v44, 5, v40
	v_add_u32_e32 v42, v44, v162
	v_ashrrev_i32_e32 v43, 31, v42
	v_lshlrev_b64 v[42:43], 5, v[42:43]
	v_lshl_add_u64 v[42:43], s[30:31], 0, v[42:43]
	v_lshl_add_u64 v[42:43], v[42:43], 0, v[136:137]
	v_ashrrev_i32_e32 v41, 31, v40
	v_lshlrev_b64 v[40:41], 12, v[40:41]
	v_lshl_add_u64 v[40:41], v[40:41], 0, s[34:35]
	s_waitcnt vmcnt(15)
	v_mov_b32_e32 v46, v232
	v_mov_b32_e32 v47, v233
	v_mov_b32_e32 v48, v234
	v_mov_b32_e32 v49, v235
	v_lshlrev_b32_e32 v42, 16, v46
	v_and_b32_e32 v43, 0xffff0000, v46
	v_pk_fma_f32 v[36:37], v[12:13], v[42:43], v[36:37]
	s_nop 0
	v_pk_mul_f32 v[42:43], v[36:37], v[36:37]
	s_nop 0
	v_fmamk_f32 v42, v42, 0xbdd2d3e8, v168
	v_fmamk_f32 v43, v43, 0xbdd2d3e8, v168
	v_mul_f32_e32 v42, v36, v42
	v_mul_f32_e32 v43, v37, v43
	v_exp_f32_e32 v42, v42
	v_exp_f32_e32 v43, v43
	v_add_f32_e32 v42, 1.0, v42
	v_add_f32_e32 v43, 1.0, v43
	v_rcp_f32_e32 v42, v42
	v_rcp_f32_e32 v43, v43
	s_nop 0
	v_pk_mul_f32 v[36:37], v[36:37], v[42:43]
	v_lshlrev_b32_e32 v42, 16, v47
	v_and_b32_e32 v43, 0xffff0000, v47
	v_pk_fma_f32 v[38:39], v[14:15], v[42:43], v[38:39]
	s_nop 0
	v_pk_mul_f32 v[42:43], v[38:39], v[38:39]
	s_nop 0
	v_fmamk_f32 v42, v42, 0xbdd2d3e8, v168
	v_fmamk_f32 v43, v43, 0xbdd2d3e8, v168
	v_mul_f32_e32 v42, v38, v42
	v_mul_f32_e32 v43, v39, v43
	v_exp_f32_e32 v42, v42
	v_exp_f32_e32 v43, v43
	v_add_f32_e32 v42, 1.0, v42
	v_add_f32_e32 v43, 1.0, v43
	v_rcp_f32_e32 v42, v42
	v_rcp_f32_e32 v43, v43
	s_nop 0
	v_pk_mul_f32 v[38:39], v[38:39], v[42:43]
	v_lshlrev_b32_e32 v42, 16, v48
	v_and_b32_e32 v43, 0xffff0000, v48
	v_pk_fma_f32 v[32:33], v[8:9], v[42:43], v[32:33]
	s_nop 0
	v_pk_mul_f32 v[42:43], v[32:33], v[32:33]
	s_nop 0
	v_fmamk_f32 v42, v42, 0xbdd2d3e8, v168
	v_fmamk_f32 v43, v43, 0xbdd2d3e8, v168
	v_mul_f32_e32 v42, v32, v42
	v_mul_f32_e32 v43, v33, v43
	v_exp_f32_e32 v42, v42
	v_exp_f32_e32 v43, v43
	v_add_f32_e32 v42, 1.0, v42
	v_add_f32_e32 v43, 1.0, v43
	v_rcp_f32_e32 v42, v42
	v_rcp_f32_e32 v43, v43
	s_nop 0
	v_pk_mul_f32 v[42:43], v[32:33], v[42:43]
	v_lshlrev_b32_e32 v32, 16, v49
	v_and_b32_e32 v33, 0xffff0000, v49
	v_pk_fma_f32 v[32:33], v[10:11], v[32:33], v[34:35]
	s_nop 0
	v_pk_mul_f32 v[34:35], v[32:33], v[32:33]
	s_nop 0
	v_fmamk_f32 v34, v34, 0xbdd2d3e8, v168
	v_fmamk_f32 v35, v35, 0xbdd2d3e8, v168
	v_mul_f32_e32 v34, v32, v34
	v_mul_f32_e32 v35, v33, v35
	v_exp_f32_e32 v34, v34
	v_exp_f32_e32 v35, v35
	v_add_f32_e32 v34, 1.0, v34
	v_add_f32_e32 v35, 1.0, v35
	v_rcp_f32_e32 v34, v34
	v_rcp_f32_e32 v35, v35
	s_nop 0
	v_pk_mul_f32 v[46:47], v[32:33], v[34:35]
	v_cvt_pk_bf16_f32 v32, v36, v37
	v_lshl_add_u64 v[36:37], v[40:41], 0, v[162:163]
	v_lshlrev_b64 v[36:37], 5, v[36:37]
	v_cvt_pk_bf16_f32 v33, v38, v39
	v_cvt_pk_bf16_f32 v34, v42, v43
	v_cvt_pk_bf16_f32 v35, v46, v47
	v_lshl_add_u64 v[36:37], v[152:153], 0, v[36:37]
	global_store_dwordx4 v[36:37], v[32:35], off
	s_nop 1
	v_add_u32_e32 v32, v44, v128
	v_ashrrev_i32_e32 v33, 31, v32
	v_lshlrev_b64 v[32:33], 5, v[32:33]
	v_lshl_add_u64 v[32:33], s[30:31], 0, v[32:33]
	v_lshl_add_u64 v[32:33], v[32:33], 0, v[136:137]
	s_waitcnt vmcnt(15)
; __device__ __forceinline__ float gelu_tanh(float x) { const float t = x * x; const float p = __builtin_fmaf(t, -0.10294324f, -2.3022082f); return x * __builtin_amdgcn_rcpf(1.0f + __builtin_amdgcn_exp2f(x * p)); }
; __device__ __forceinline__ u32x4 pack8(const float (&v)[8]) { u32x4 w; w.x = pk2(v[0], v[1]); w.y = pk2(v[2], v[3]); w.z = pk2(v[4], v[5]); w.w = pk2(v[6], v[7]); return w; }
;     __device__ __forceinline__ void operator()(const f32x4 (&acc)[2][2][4][2], const pg::Unit& u, int wr, int wc, int fr, int fq) const {
;         const int g = u.e, ch0 = (fq & 1) * 8; float dv[8];
; #pragma unroll
;         for (int q = 0; q < 8; ++q) dv[q] = dsk[g * 16 + ch0 + q];
; #pragma unroll
;         for (int ai = 0; ai < 2; ++ai)
; #pragma unroll
;             for (int m = 0; m < 4; ++m) { const int n = u.pm * 256 + ai * 128 + wr * 64 + m * 16 + fr;
; #pragma unroll
;                 for (int bj = 0; bj < 2; ++bj) { const int t = u.pn * 16 + 8 * bj + 2 * wc + (fq >> 1); const int token = n * 32 + t;
;                     float uu[8], o[8]; unpack8(*(const u32x4*)(U2 + ((size_t)g * T_ + token) * 16 + ch0), uu);
; #pragma unroll
;                     for (int q = 0; q < 8; ++q) o[q] = gelu_tanh(acc[ai][bj][m][q >> 2][q & 3] + dv[q] * uu[q]);
;                     *(u32x4*)(V + (((size_t)n * 128 + g) * 32 + t) * 16 + ch0) = pack8(o); } }
	v_mov_b32_e32 v32, v236
	v_mov_b32_e32 v33, v237
	v_mov_b32_e32 v34, v238
	v_mov_b32_e32 v35, v239
	v_lshlrev_b32_e32 v36, 16, v32
	v_and_b32_e32 v37, 0xffff0000, v32
	v_pk_fma_f32 v[28:29], v[12:13], v[36:37], v[28:29]
	s_nop 0
	v_pk_mul_f32 v[36:37], v[28:29], v[28:29]
	s_nop 0
	v_fmamk_f32 v32, v36, 0xbdd2d3e8, v168
	v_mul_f32_e32 v32, v28, v32
	v_exp_f32_e32 v32, v32
	s_nop 0
	v_add_f32_e32 v32, 1.0, v32
	v_rcp_f32_e32 v36, v32
	v_fmamk_f32 v32, v37, 0xbdd2d3e8, v168
	v_mul_f32_e32 v32, v29, v32
	v_exp_f32_e32 v32, v32
	s_nop 0
	v_add_f32_e32 v32, 1.0, v32
	v_rcp_f32_e32 v37, v32
	v_lshlrev_b32_e32 v32, 16, v33
	v_and_b32_e32 v33, 0xffff0000, v33
	v_pk_fma_f32 v[30:31], v[14:15], v[32:33], v[30:31]
	v_pk_mul_f32 v[28:29], v[28:29], v[36:37]
	v_pk_mul_f32 v[32:33], v[30:31], v[30:31]
	s_nop 0
	v_fmamk_f32 v32, v32, 0xbdd2d3e8, v168
	v_fmamk_f32 v33, v33, 0xbdd2d3e8, v168
	v_mul_f32_e32 v32, v30, v32
	v_mul_f32_e32 v33, v31, v33
	v_exp_f32_e32 v32, v32
	v_exp_f32_e32 v33, v33
	v_add_f32_e32 v32, 1.0, v32
	v_add_f32_e32 v33, 1.0, v33
	v_rcp_f32_e32 v32, v32
	v_rcp_f32_e32 v33, v33
	s_nop 0
	v_pk_mul_f32 v[30:31], v[30:31], v[32:33]
	v_lshlrev_b32_e32 v32, 16, v34
	v_and_b32_e32 v33, 0xffff0000, v34
	v_pk_fma_f32 v[24:25], v[8:9], v[32:33], v[24:25]
	s_nop 0
	v_pk_mul_f32 v[32:33], v[24:25], v[24:25]
	s_nop 0
	v_fmamk_f32 v32, v32, 0xbdd2d3e8, v168
	v_fmamk_f32 v33, v33, 0xbdd2d3e8, v168
	v_mul_f32_e32 v32, v24, v32
	v_mul_f32_e32 v33, v25, v33
	v_exp_f32_e32 v32, v32
	v_exp_f32_e32 v33, v33
	v_add_f32_e32 v32, 1.0, v32
	v_add_f32_e32 v33, 1.0, v33
	v_rcp_f32_e32 v32, v32
	v_rcp_f32_e32 v33, v33
	s_nop 0
	v_pk_mul_f32 v[32:33], v[24:25], v[32:33]
	v_lshlrev_b32_e32 v24, 16, v35
	v_and_b32_e32 v25, 0xffff0000, v35
	v_pk_fma_f32 v[24:25], v[10:11], v[24:25], v[26:27]
	s_nop 0
	v_pk_mul_f32 v[26:27], v[24:25], v[24:25]
	s_nop 0
	v_fmamk_f32 v26, v26, 0xbdd2d3e8, v168
	v_fmamk_f32 v27, v27, 0xbdd2d3e8, v168
	v_mul_f32_e32 v26, v24, v26
	v_mul_f32_e32 v27, v25, v27
	v_exp_f32_e32 v26, v26
	v_exp_f32_e32 v27, v27
	v_add_f32_e32 v26, 1.0, v26
	v_add_f32_e32 v27, 1.0, v27
	v_rcp_f32_e32 v26, v26
	v_rcp_f32_e32 v27, v27
	s_nop 0
	v_pk_mul_f32 v[34:35], v[24:25], v[26:27]
	v_cvt_pk_bf16_f32 v24, v28, v29
	v_lshl_add_u64 v[28:29], v[40:41], 0, v[128:129]
	v_lshlrev_b64 v[28:29], 5, v[28:29]
	v_cvt_pk_bf16_f32 v25, v30, v31
	v_cvt_pk_bf16_f32 v26, v32, v33
	v_cvt_pk_bf16_f32 v27, v34, v35
	v_lshl_add_u64 v[28:29], v[152:153], 0, v[28:29]
	global_store_dwordx4 v[28:29], v[24:27], off
	s_nop 1
	v_add_u32_e32 v24, 0xb0, v164
	v_lshlrev_b32_e32 v28, 5, v24
	v_add_u32_e32 v26, v28, v162
	v_ashrrev_i32_e32 v27, 31, v26
	v_lshlrev_b64 v[26:27], 5, v[26:27]
	v_lshl_add_u64 v[26:27], s[30:31], 0, v[26:27]
	v_lshl_add_u64 v[26:27], v[26:27], 0, v[136:137]
	v_ashrrev_i32_e32 v25, 31, v24
	v_lshlrev_b64 v[24:25], 12, v[24:25]
	v_lshl_add_u64 v[24:25], v[24:25], 0, s[34:35]
	s_waitcnt vmcnt(15)
; __device__ __forceinline__ float gelu_tanh(float x) { const float t = x * x; const float p = __builtin_fmaf(t, -0.10294324f, -2.3022082f); return x * __builtin_amdgcn_rcpf(1.0f + __builtin_amdgcn_exp2f(x * p)); }
; __device__ __forceinline__ u32x4 pack8(const float (&v)[8]) { u32x4 w; w.x = pk2(v[0], v[1]); w.y = pk2(v[2], v[3]); w.z = pk2(v[4], v[5]); w.w = pk2(v[6], v[7]); return w; }
;     __device__ __forceinline__ void operator()(const f32x4 (&acc)[2][2][4][2], const pg::Unit& u, int wr, int wc, int fr, int fq) const {
;         const int g = u.e, ch0 = (fq & 1) * 8; float dv[8];
; #pragma unroll
;         for (int q = 0; q < 8; ++q) dv[q] = dsk[g * 16 + ch0 + q];
; #pragma unroll
;         for (int ai = 0; ai < 2; ++ai)
; #pragma unroll
;             for (int m = 0; m < 4; ++m) { const int n = u.pm * 256 + ai * 128 + wr * 64 + m * 16 + fr;
; #pragma unroll
;                 for (int bj = 0; bj < 2; ++bj) { const int t = u.pn * 16 + 8 * bj + 2 * wc + (fq >> 1); const int token = n * 32 + t;
;                     float uu[8], o[8]; unpack8(*(const u32x4*)(U2 + ((size_t)g * T_ + token) * 16 + ch0), uu);
; #pragma unroll
;                     for (int q = 0; q < 8; ++q) o[q] = gelu_tanh(acc[ai][bj][m][q >> 2][q & 3] + dv[q] * uu[q]);
;                     *(u32x4*)(V + (((size_t)n * 128 + g) * 32 + t) * 16 + ch0) = pack8(o); } }
	v_mov_b32_e32 v30, v240
	v_mov_b32_e32 v31, v241
	v_mov_b32_e32 v32, v242
	v_mov_b32_e32 v33, v243
	v_lshlrev_b32_e32 v26, 16, v30
	v_and_b32_e32 v27, 0xffff0000, v30
	v_pk_fma_f32 v[20:21], v[12:13], v[26:27], v[20:21]
	s_nop 0
	v_pk_mul_f32 v[26:27], v[20:21], v[20:21]
	s_nop 0
	v_fmamk_f32 v26, v26, 0xbdd2d3e8, v168
	v_fmamk_f32 v27, v27, 0xbdd2d3e8, v168
	v_mul_f32_e32 v26, v20, v26
	v_mul_f32_e32 v27, v21, v27
	v_exp_f32_e32 v26, v26
	v_exp_f32_e32 v27, v27
	v_add_f32_e32 v26, 1.0, v26
	v_add_f32_e32 v27, 1.0, v27
	v_rcp_f32_e32 v26, v26
	v_rcp_f32_e32 v27, v27
	s_nop 0
	v_pk_mul_f32 v[20:21], v[20:21], v[26:27]
	v_lshlrev_b32_e32 v26, 16, v31
	v_and_b32_e32 v27, 0xffff0000, v31
	v_pk_fma_f32 v[22:23], v[14:15], v[26:27], v[22:23]
	s_nop 0
	v_pk_mul_f32 v[26:27], v[22:23], v[22:23]
	s_nop 0
	v_fmamk_f32 v26, v26, 0xbdd2d3e8, v168
	v_fmamk_f32 v27, v27, 0xbdd2d3e8, v168
	v_mul_f32_e32 v26, v22, v26
	v_mul_f32_e32 v27, v23, v27
	v_exp_f32_e32 v26, v26
	v_exp_f32_e32 v27, v27
	v_add_f32_e32 v26, 1.0, v26
	v_add_f32_e32 v27, 1.0, v27
	v_rcp_f32_e32 v26, v26
	v_rcp_f32_e32 v27, v27
	s_nop 0
	v_pk_mul_f32 v[22:23], v[22:23], v[26:27]
	v_lshlrev_b32_e32 v26, 16, v32
	v_and_b32_e32 v27, 0xffff0000, v32
	v_pk_fma_f32 v[16:17], v[8:9], v[26:27], v[16:17]
	s_nop 0
	v_pk_mul_f32 v[26:27], v[16:17], v[16:17]
	s_nop 0
	v_fmamk_f32 v26, v26, 0xbdd2d3e8, v168
	v_fmamk_f32 v27, v27, 0xbdd2d3e8, v168
	v_mul_f32_e32 v26, v16, v26
	v_mul_f32_e32 v27, v17, v27
	v_exp_f32_e32 v26, v26
	v_exp_f32_e32 v27, v27
	v_add_f32_e32 v26, 1.0, v26
	v_add_f32_e32 v27, 1.0, v27
	v_rcp_f32_e32 v26, v26
	v_rcp_f32_e32 v27, v27
	s_nop 0
	v_pk_mul_f32 v[26:27], v[16:17], v[26:27]
	v_lshlrev_b32_e32 v16, 16, v33
	v_and_b32_e32 v17, 0xffff0000, v33
	v_pk_fma_f32 v[16:17], v[10:11], v[16:17], v[18:19]
	s_nop 0
	v_pk_mul_f32 v[18:19], v[16:17], v[16:17]
	s_nop 0
	v_fmamk_f32 v18, v18, 0xbdd2d3e8, v168
	v_fmamk_f32 v19, v19, 0xbdd2d3e8, v168
	v_mul_f32_e32 v18, v16, v18
	v_mul_f32_e32 v19, v17, v19
	v_exp_f32_e32 v18, v18
	v_exp_f32_e32 v19, v19
	v_add_f32_e32 v18, 1.0, v18
	v_add_f32_e32 v19, 1.0, v19
	v_rcp_f32_e32 v18, v18
	v_rcp_f32_e32 v19, v19
	s_nop 0
	v_pk_mul_f32 v[30:31], v[16:17], v[18:19]
	v_cvt_pk_bf16_f32 v16, v20, v21
	v_lshl_add_u64 v[20:21], v[24:25], 0, v[162:163]
	v_lshlrev_b64 v[20:21], 5, v[20:21]
	v_cvt_pk_bf16_f32 v17, v22, v23
	v_cvt_pk_bf16_f32 v18, v26, v27
	v_cvt_pk_bf16_f32 v19, v30, v31
	v_lshl_add_u64 v[20:21], v[152:153], 0, v[20:21]
	global_store_dwordx4 v[20:21], v[16:19], off
	s_nop 1
	v_add_u32_e32 v16, v28, v128
	v_ashrrev_i32_e32 v17, 31, v16
	v_lshlrev_b64 v[16:17], 5, v[16:17]
	v_lshl_add_u64 v[16:17], s[30:31], 0, v[16:17]
	v_lshl_add_u64 v[16:17], v[16:17], 0, v[136:137]
	s_mov_b64 s[30:31], -1
	s_waitcnt vmcnt(15)
	v_mov_b32_e32 v16, v244
	v_mov_b32_e32 v17, v245
	v_mov_b32_e32 v18, v246
	v_mov_b32_e32 v19, v247
	v_lshlrev_b32_e32 v20, 16, v16
	v_and_b32_e32 v21, 0xffff0000, v16
	v_pk_fma_f32 v[4:5], v[12:13], v[20:21], v[4:5]
	s_nop 0
	v_pk_mul_f32 v[12:13], v[4:5], v[4:5]
	s_nop 0
	v_fmamk_f32 v12, v12, 0xbdd2d3e8, v168
	v_fmamk_f32 v13, v13, 0xbdd2d3e8, v168
	v_mul_f32_e32 v12, v4, v12
	v_mul_f32_e32 v13, v5, v13
	v_exp_f32_e32 v12, v12
	v_exp_f32_e32 v13, v13
	v_add_f32_e32 v12, 1.0, v12
	v_add_f32_e32 v13, 1.0, v13
	v_rcp_f32_e32 v12, v12
	v_rcp_f32_e32 v13, v13
	s_nop 0
	v_pk_mul_f32 v[4:5], v[4:5], v[12:13]
	v_lshlrev_b32_e32 v12, 16, v17
	v_and_b32_e32 v13, 0xffff0000, v17
	v_pk_fma_f32 v[6:7], v[14:15], v[12:13], v[6:7]
	s_nop 0
	v_pk_mul_f32 v[12:13], v[6:7], v[6:7]
	s_nop 0
	v_fmamk_f32 v12, v12, 0xbdd2d3e8, v168
	v_fmamk_f32 v13, v13, 0xbdd2d3e8, v168
	v_mul_f32_e32 v12, v6, v12
	v_mul_f32_e32 v13, v7, v13
	v_exp_f32_e32 v12, v12
	v_exp_f32_e32 v13, v13
	v_add_f32_e32 v12, 1.0, v12
	v_add_f32_e32 v13, 1.0, v13
	v_rcp_f32_e32 v12, v12
	v_rcp_f32_e32 v13, v13
	s_nop 0
	v_pk_mul_f32 v[6:7], v[6:7], v[12:13]
	v_lshlrev_b32_e32 v12, 16, v18
	v_and_b32_e32 v13, 0xffff0000, v18
	v_pk_fma_f32 v[0:1], v[8:9], v[12:13], v[0:1]
	s_nop 0
	v_pk_mul_f32 v[8:9], v[0:1], v[0:1]
	s_nop 0
	v_fmamk_f32 v8, v8, 0xbdd2d3e8, v168
	v_fmamk_f32 v9, v9, 0xbdd2d3e8, v168
	v_mul_f32_e32 v8, v0, v8
	v_mul_f32_e32 v9, v1, v9
	v_exp_f32_e32 v8, v8
	v_exp_f32_e32 v9, v9
	v_add_f32_e32 v8, 1.0, v8
	v_add_f32_e32 v9, 1.0, v9
	v_rcp_f32_e32 v8, v8
	v_rcp_f32_e32 v9, v9
	s_nop 0
	v_pk_mul_f32 v[8:9], v[0:1], v[8:9]
	v_lshlrev_b32_e32 v0, 16, v19
	v_and_b32_e32 v1, 0xffff0000, v19
	v_pk_fma_f32 v[0:1], v[10:11], v[0:1], v[2:3]
	s_nop 0
	v_pk_mul_f32 v[2:3], v[0:1], v[0:1]
	s_nop 0
	v_fmamk_f32 v2, v2, 0xbdd2d3e8, v168
	v_fmamk_f32 v3, v3, 0xbdd2d3e8, v168
	v_mul_f32_e32 v2, v0, v2
	v_mul_f32_e32 v3, v1, v3
	v_exp_f32_e32 v2, v2
	v_exp_f32_e32 v3, v3
	v_add_f32_e32 v2, 1.0, v2
	v_add_f32_e32 v3, 1.0, v3
	v_rcp_f32_e32 v2, v2
	v_rcp_f32_e32 v3, v3
	s_nop 0
	v_pk_mul_f32 v[10:11], v[0:1], v[2:3]
	v_cvt_pk_bf16_f32 v0, v4, v5
	v_lshl_add_u64 v[4:5], v[24:25], 0, v[128:129]
	v_lshlrev_b64 v[4:5], 5, v[4:5]
	v_cvt_pk_bf16_f32 v1, v6, v7
	v_cvt_pk_bf16_f32 v2, v8, v9
	v_cvt_pk_bf16_f32 v3, v10, v11
	v_lshl_add_u64 v[4:5], v[152:153], 0, v[4:5]
	global_store_dwordx4 v[4:5], v[0:3], off
	s_cbranch_vccnz .LBB0_1770
	s_and_b64 vcc, exec, s[0:1]
	s_cbranch_vccnz .LBB0_1769
	s_barrier
	s_branch .LBB0_1769
